# speedup vs baseline: 1.0194x; 1.0194x over previous
_Z16closed_form_mainPKfS0_PKiPf:
	s_load_dwordx8 s[16:23], s[0:1], 0x0
	s_lshr_b32 s6, s2, 3
	v_readfirstlane_b32 s0, v0
	s_mul_hi_u32 s7, s6, 0x24924925
	s_lshr_b32 s4, s0, 6
	s_and_b32 s0, s2, 7
	s_mul_i32 s1, s7, 7
	s_bfe_u32 s5, s2, 0x10003
	s_sub_i32 s1, s6, s1
	s_mul_i32 s36, s0, 7
	s_xor_b32 s3, s4, s5
	s_add_i32 s36, s36, s1
	s_waitcnt lgkmcnt(0)
	s_mov_b64 s[28:29], s[22:23]
	v_and_b32_e32 v19, 63, v0
	s_cmp_lt_u32 s36, 52
	s_mov_b64 s[0:1], -1
	s_cbranch_scc0 .LBB0_32
	s_mul_hi_u32 s0, s6, 0x20820821
	s_lshr_b32 s38, s0, 3
	s_mul_hi_u32 s0, s7, 0x1c71c71d
	s_mul_i32 s0, s0, 9
	s_sub_i32 s0, s7, s0
	v_add_u32_e32 v2, -3, v19
	v_mad_u64_u32 v[0:1], s[0:1], s0, 57, v[2:3]
	s_mov_b64 s[24:25], s[18:19]
	v_mov_b32_e32 v1, 0x200
	v_med3_i32 v1, v0, 0, v1
	s_mul_i32 s34, s36, 10
	s_and_b32 s17, s17, 0xffff
	s_and_b32 s25, s25, 0xffff
	v_cmp_gt_u32_e64 s[0:1], 57, v2
	s_mov_b32 s19, 0x20000
	s_mov_b32 s18, 0xe0e038
	s_mov_b32 s26, 0x606018
	s_mul_i32 s35, s38, 0x70701c
	s_mul_i32 s33, s38, 0x30300c
	v_lshlrev_b32_e32 v28, 2, v1
	v_mul_u32_u24_e32 v27, 12, v1
	v_lshlrev_b32_e32 v23, 4, v19
	s_cmp_lg_u32 s4, s5
	v_sub_u32_e64 v29, s34, 2 clamp
	s_cbranch_scc0 .LBB0_15
	s_setprio 2
	s_mov_b32 s27, s19
	s_and_b32 s21, s21, 0xffff
	s_mov_b32 s22, 0x202008
	s_mov_b32 s23, s19
	s_mul_i32 s38, s38, 0x101004
	s_movk_i32 s37, 0x80
	v_add_u32_e32 v18, -1, v0
	s_movk_i32 s4, 0x201
	s_movk_i32 s5, 0x1ff
	v_cmp_gt_u32_e64 s[40:41], s4, v0
	v_cmp_gt_u32_e64 s[42:43], s5, v18
	v_mov_b32_e32 v18, 0x42c80000
	v_mov_b32_e32 v22, 0x3de38e39
	v_mov_b32_e32 v26, 0x3a3d6628
	v_mov_b32_e32 v1, 0
	s_add_i32 s4, s34, -3
	s_max_i32 s4, s4, 0
	s_mul_i32 s4, s4, 0x804
	s_add_i32 s4, s4, s38
	buffer_load_dword v29, v28, s[20:23], s4 offen nt
	s_add_i32 s4, s34, -2
	s_max_i32 s4, s4, 0
	s_mul_i32 s4, s4, 0x804
	s_add_i32 s4, s4, s38
	buffer_load_dword v2, v28, s[20:23], s4 offen nt
	s_add_i32 s5, s34, -2
	s_max_i32 s5, s5, 0
	s_mul_i32 s6, s5, 0x804
	s_add_i32 s6, s6, s35
	s_add_i32 s7, s6, 0x505014
	s_add_i32 s8, s6, 0x606018
	s_mul_i32 s9, s5, 0x180c
	s_add_i32 s9, s9, s33
	s_add_i32 s4, s34, -1
	s_max_i32 s4, s4, 0
	s_mul_i32 s4, s4, 0x804
	s_add_i32 s4, s4, s38
	buffer_load_dword v3, v28, s[20:23], s4 offen nt
	buffer_load_dwordx3 v[8:10], v27, s[24:27], s9 offen nt
	buffer_load_dword v4, v28, s[16:19], s7 offen nt
	buffer_load_dword v5, v28, s[16:19], s8 offen nt
	s_add_i32 s5, s34, -1
	s_max_i32 s5, s5, 0
	s_mul_i32 s6, s5, 0x804
	s_add_i32 s6, s6, s35
	s_add_i32 s7, s6, 0x505014
	s_add_i32 s8, s6, 0x606018
	s_mul_i32 s9, s5, 0x180c
	s_add_i32 s9, s9, s33
	s_add_i32 s4, s34, 0
	s_min_i32 s4, s4, 0x200
	s_mul_i32 s4, s4, 0x804
	s_add_i32 s4, s4, s38
	buffer_load_dword v16, v28, s[20:23], s4 offen nt
	buffer_load_dwordx3 v[12:14], v27, s[24:27], s9 offen nt
	buffer_load_dword v6, v28, s[16:19], s7 offen nt
	buffer_load_dword v7, v28, s[16:19], s8 offen nt
	s_waitcnt vmcnt(8)
	s_add_i32 s4, s34, -3
	s_cmpk_lt_u32 s4, 0x201
	s_cselect_b64 s[12:13], s[40:41], 0
	v_cmp_eq_u32_e64 s[14:15], s37, v29
	s_and_b64 s[14:15], s[14:15], s[12:13]
	v_cndmask_b32_e64 v17, 0, 1, s[14:15]
	s_add_i32 s4, s34, -2
	s_cmpk_lt_u32 s4, 0x201
	s_cselect_b64 s[12:13], s[40:41], 0
	v_cmp_eq_u32_e64 s[14:15], s37, v2
	s_and_b64 s[14:15], s[14:15], s[12:13]
	v_cndmask_b32_e64 v20, 0, 1, s[14:15]
	s_nop 0
	v_or_b32_dpp v21, v17, v17 wave_shr:1 row_mask:0xf bank_mask:0xf bound_ctrl:1
	v_or_b32_dpp v24, v20, v20 wave_shr:1 row_mask:0xf bank_mask:0xf bound_ctrl:1
	s_nop 1
	v_or_b32_dpp v21, v17, v21 wave_shl:1 row_mask:0xf bank_mask:0xf bound_ctrl:1
	v_or_b32_dpp v24, v20, v24 wave_shl:1 row_mask:0xf bank_mask:0xf bound_ctrl:1
	s_nop 1
	v_or_b32_dpp v25, v21, v21 wave_shr:1 row_mask:0xf bank_mask:0xf bound_ctrl:1
	v_or_b32_dpp v30, v24, v24 wave_shr:1 row_mask:0xf bank_mask:0xf bound_ctrl:1
	s_nop 1
	v_or_b32_dpp v25, v21, v25 wave_shl:1 row_mask:0xf bank_mask:0xf bound_ctrl:1
	v_or_b32_dpp v30, v24, v30 wave_shl:1 row_mask:0xf bank_mask:0xf bound_ctrl:1
	v_mov_b32_e32 v17, 0
	v_mov_b32_e32 v24, 0
	s_add_i32 s5, s34, 0
	s_min_i32 s5, s5, 0x200
	s_mul_i32 s6, s5, 0x804
	s_add_i32 s6, s6, s35
	s_add_i32 s7, s6, 0x505014
	s_add_i32 s8, s6, 0x606018
	s_mul_i32 s9, s5, 0x180c
	s_add_i32 s9, s9, s33
	s_add_i32 s4, s34, 1
	s_min_i32 s4, s4, 0x200
	s_mul_i32 s4, s4, 0x804
	s_add_i32 s4, s4, s38
	buffer_load_dword v31, v28, s[20:23], s4 offen nt
	buffer_load_dwordx3 v[32:34], v27, s[24:27], s9 offen nt
	buffer_load_dword v20, v28, s[16:19], s7 offen nt
	buffer_load_dword v21, v28, s[16:19], s8 offen nt
	s_waitcnt vmcnt(8)
	v_mov_b32_dpp v36, v8 wave_shr:1 row_mask:0xf bank_mask:0xf bound_ctrl:1
	v_mov_b32_dpp v37, v9 wave_shr:1 row_mask:0xf bank_mask:0xf bound_ctrl:1
	v_mov_b32_dpp v38, v10 wave_shr:1 row_mask:0xf bank_mask:0xf bound_ctrl:1
	v_mov_b32_dpp v40, v8 wave_shl:1 row_mask:0xf bank_mask:0xf bound_ctrl:1
	v_mov_b32_dpp v41, v9 wave_shl:1 row_mask:0xf bank_mask:0xf bound_ctrl:1
	v_mov_b32_dpp v42, v10 wave_shl:1 row_mask:0xf bank_mask:0xf bound_ctrl:1
	s_add_i32 s4, s34, -1
	s_cmpk_lt_u32 s4, 0x201
	s_cselect_b64 s[12:13], s[40:41], 0
	v_cmp_eq_u32_e64 s[14:15], s37, v3
	s_and_b64 s[14:15], s[14:15], s[12:13]
	v_cndmask_b32_e64 v44, 0, 1, s[14:15]
	v_mul_f32_e64 v46, v8, v8
	v_mul_f32_e64 v47, v8, v9
	v_mul_f32_e64 v48, v8, v10
	v_mul_f32_e64 v49, v9, v9
	v_mul_f32_e64 v50, v9, v10
	v_mul_f32_e64 v51, v10, v10
	v_or_b32_dpp v45, v44, v44 wave_shr:1 row_mask:0xf bank_mask:0xf bound_ctrl:1
	s_nop 1
	v_or_b32_dpp v45, v44, v45 wave_shl:1 row_mask:0xf bank_mask:0xf bound_ctrl:1
	s_nop 1
	v_or_b32_dpp v52, v45, v45 wave_shr:1 row_mask:0xf bank_mask:0xf bound_ctrl:1
	s_nop 1
	v_or_b32_dpp v52, v45, v52 wave_shl:1 row_mask:0xf bank_mask:0xf bound_ctrl:1
	v_or3_b32 v53, v52, v30, v25
	v_or3_b32 v53, v53, v17, v24
	s_add_i32 s4, s34, -4
	s_cmpk_lt_u32 s4, 0x1ff
	s_cselect_b64 s[12:13], s[42:43], 0
	v_cmp_ne_u32_e64 s[30:31], 0, v53
	s_and_b64 s[30:31], s[30:31], s[12:13]
	v_cndmask_b32_e64 v53, 0, 1.0, s[30:31]
	v_add_f32_e64 v44, v8, v36
	v_add_f32_e64 v45, v9, v37
	v_add_f32_e64 v54, v10, v38
	v_fma_f32 v46, v36, v36, v46
	v_fma_f32 v47, v36, v37, v47
	v_fma_f32 v48, v36, v38, v48
	v_fma_f32 v49, v37, v37, v49
	v_fma_f32 v50, v37, v38, v50
	v_fma_f32 v51, v38, v38, v51
	v_add_f32_dpp v61, v53, v53 wave_shr:1 row_mask:0xf bank_mask:0xf bound_ctrl:1
	v_add_f32_e64 v44, v44, v40
	v_add_f32_e64 v45, v45, v41
	v_add_f32_e64 v54, v54, v42
	v_fma_f32 v55, v40, v40, v46
	v_fma_f32 v56, v40, v41, v47
	v_fma_f32 v57, v40, v42, v48
	v_fma_f32 v58, v41, v41, v49
	v_fma_f32 v59, v41, v42, v50
	v_fma_f32 v60, v42, v42, v51
	v_add_f32_dpp v61, v53, v61 wave_shl:1 row_mask:0xf bank_mask:0xf bound_ctrl:1
	s_barrier
	v_mov_b32_dpp v46, v4 wave_shr:1 row_mask:0xf bank_mask:0xf bound_ctrl:1
	v_mov_b32_dpp v47, v5 wave_shr:1 row_mask:0xf bank_mask:0xf bound_ctrl:1
	v_mov_b32_dpp v48, v4 wave_shl:1 row_mask:0xf bank_mask:0xf bound_ctrl:1
	v_mov_b32_dpp v49, v5 wave_shl:1 row_mask:0xf bank_mask:0xf bound_ctrl:1
	v_pk_mul_f32 v[50:51], v[4:5], v[8:9] op_sel_hi:[1,0]
	v_pk_mul_f32 v[62:63], v[4:5], v[8:9] op_sel:[0,1]
	v_pk_mul_f32 v[64:65], v[4:5], v[10:11] op_sel_hi:[1,0]
	v_pk_add_f32 v[66:67], v[4:5], v[46:47]
	v_pk_fma_f32 v[50:51], v[46:47], v[36:37], v[50:51] op_sel_hi:[1,0,1]
	v_pk_fma_f32 v[62:63], v[46:47], v[36:37], v[62:63] op_sel:[0,1,0]
	v_pk_fma_f32 v[64:65], v[46:47], v[38:39], v[64:65] op_sel_hi:[1,0,1]
	v_pk_add_f32 v[66:67], v[66:67], v[48:49]
	v_pk_fma_f32 v[50:51], v[48:49], v[40:41], v[50:51] op_sel_hi:[1,0,1]
	v_pk_fma_f32 v[62:63], v[48:49], v[40:41], v[62:63] op_sel:[0,1,0]
	v_pk_fma_f32 v[64:65], v[48:49], v[42:43], v[64:65] op_sel_hi:[1,0,1]
	s_add_i32 s5, s34, 1
	s_min_i32 s5, s5, 0x200
	s_mul_i32 s6, s5, 0x804
	s_add_i32 s6, s6, s35
	s_add_i32 s7, s6, 0x505014
	s_add_i32 s8, s6, 0x606018
	s_mul_i32 s9, s5, 0x180c
	s_add_i32 s9, s9, s33
	s_add_i32 s4, s34, 2
	s_min_i32 s4, s4, 0x200
	s_mul_i32 s4, s4, 0x804
	s_add_i32 s4, s4, s38
	buffer_load_dword v24, v28, s[20:23], s4 offen nt
	buffer_load_dwordx3 v[68:70], v27, s[24:27], s9 offen nt
	buffer_load_dword v46, v28, s[16:19], s7 offen nt
	buffer_load_dword v47, v28, s[16:19], s8 offen nt
	s_waitcnt vmcnt(8)
	v_mov_b32_dpp v72, v12 wave_shr:1 row_mask:0xf bank_mask:0xf bound_ctrl:1
	v_mov_b32_dpp v73, v13 wave_shr:1 row_mask:0xf bank_mask:0xf bound_ctrl:1
	v_mov_b32_dpp v74, v14 wave_shr:1 row_mask:0xf bank_mask:0xf bound_ctrl:1
	v_mov_b32_dpp v76, v12 wave_shl:1 row_mask:0xf bank_mask:0xf bound_ctrl:1
	v_mov_b32_dpp v77, v13 wave_shl:1 row_mask:0xf bank_mask:0xf bound_ctrl:1
	v_mov_b32_dpp v78, v14 wave_shl:1 row_mask:0xf bank_mask:0xf bound_ctrl:1
	s_add_i32 s4, s34, 0
	s_cmpk_lt_u32 s4, 0x201
	s_cselect_b64 s[12:13], s[40:41], 0
	v_cmp_eq_u32_e64 s[14:15], s37, v16
	s_and_b64 s[14:15], s[14:15], s[12:13]
	v_cndmask_b32_e64 v53, 0, 1, s[14:15]
	v_mul_f32_e64 v48, v12, v12
	v_mul_f32_e64 v49, v12, v13
	v_mul_f32_e64 v80, v12, v14
	v_mul_f32_e64 v81, v13, v13
	v_mul_f32_e64 v82, v13, v14
	v_mul_f32_e64 v83, v14, v14
	v_or_b32_dpp v84, v53, v53 wave_shr:1 row_mask:0xf bank_mask:0xf bound_ctrl:1
	s_nop 1
	v_or_b32_dpp v84, v53, v84 wave_shl:1 row_mask:0xf bank_mask:0xf bound_ctrl:1
	s_nop 1
	v_or_b32_dpp v85, v84, v84 wave_shr:1 row_mask:0xf bank_mask:0xf bound_ctrl:1
	s_nop 1
	v_or_b32_dpp v85, v84, v85 wave_shl:1 row_mask:0xf bank_mask:0xf bound_ctrl:1
	v_or3_b32 v53, v85, v52, v30
	v_or3_b32 v53, v53, v25, v17
	s_add_i32 s4, s34, -3
	s_cmpk_lt_u32 s4, 0x1ff
	s_cselect_b64 s[12:13], s[42:43], 0
	v_cmp_ne_u32_e64 s[30:31], 0, v53
	s_and_b64 s[30:31], s[30:31], s[12:13]
	v_cndmask_b32_e64 v53, 0, 1.0, s[30:31]
	v_add_f32_e64 v86, v12, v72
	v_add_f32_e64 v87, v13, v73
	v_add_f32_e64 v88, v14, v74
	v_fma_f32 v48, v72, v72, v48
	v_fma_f32 v49, v72, v73, v49
	v_fma_f32 v80, v72, v74, v80
	v_fma_f32 v81, v73, v73, v81
	v_fma_f32 v82, v73, v74, v82
	v_fma_f32 v83, v74, v74, v83
	v_add_f32_dpp v95, v53, v53 wave_shr:1 row_mask:0xf bank_mask:0xf bound_ctrl:1
	v_add_f32_e64 v86, v86, v76
	v_add_f32_e64 v87, v87, v77
	v_add_f32_e64 v88, v88, v78
	v_fma_f32 v89, v76, v76, v48
	v_fma_f32 v90, v76, v77, v49
	v_fma_f32 v91, v76, v78, v80
	v_fma_f32 v92, v77, v77, v81
	v_fma_f32 v93, v77, v78, v82
	v_fma_f32 v94, v78, v78, v83
	v_add_f32_dpp v95, v53, v95 wave_shl:1 row_mask:0xf bank_mask:0xf bound_ctrl:1
	s_barrier
	v_mov_b32_dpp v48, v6 wave_shr:1 row_mask:0xf bank_mask:0xf bound_ctrl:1
	v_mov_b32_dpp v49, v7 wave_shr:1 row_mask:0xf bank_mask:0xf bound_ctrl:1
	v_mov_b32_dpp v80, v6 wave_shl:1 row_mask:0xf bank_mask:0xf bound_ctrl:1
	v_mov_b32_dpp v81, v7 wave_shl:1 row_mask:0xf bank_mask:0xf bound_ctrl:1
	v_pk_mul_f32 v[82:83], v[6:7], v[12:13] op_sel_hi:[1,0]
	v_pk_mul_f32 v[96:97], v[6:7], v[12:13] op_sel:[0,1]
	v_pk_mul_f32 v[98:99], v[6:7], v[14:15] op_sel_hi:[1,0]
	v_pk_add_f32 v[100:101], v[6:7], v[48:49]
	v_pk_fma_f32 v[82:83], v[48:49], v[72:73], v[82:83] op_sel_hi:[1,0,1]
	v_pk_fma_f32 v[96:97], v[48:49], v[72:73], v[96:97] op_sel:[0,1,0]
	v_pk_fma_f32 v[98:99], v[48:49], v[74:75], v[98:99] op_sel_hi:[1,0,1]
	v_pk_add_f32 v[100:101], v[100:101], v[80:81]
	v_pk_fma_f32 v[82:83], v[80:81], v[76:77], v[82:83] op_sel_hi:[1,0,1]
	v_pk_fma_f32 v[96:97], v[80:81], v[76:77], v[96:97] op_sel:[0,1,0]
	v_pk_fma_f32 v[98:99], v[80:81], v[78:79], v[98:99] op_sel_hi:[1,0,1]
	s_add_i32 s5, s34, 2
	s_min_i32 s5, s5, 0x200
	s_mul_i32 s6, s5, 0x804
	s_add_i32 s6, s6, s35
	s_add_i32 s7, s6, 0x505014
	s_add_i32 s8, s6, 0x606018
	s_mul_i32 s9, s5, 0x180c
	s_add_i32 s9, s9, s33
	s_add_i32 s4, s34, 3
	s_min_i32 s4, s4, 0x200
	s_mul_i32 s4, s4, 0x804
	s_add_i32 s4, s4, s38
	buffer_load_dword v17, v28, s[20:23], s4 offen nt
	buffer_load_dwordx3 v[104:106], v27, s[24:27], s9 offen nt
	buffer_load_dword v48, v28, s[16:19], s7 offen nt
	buffer_load_dword v49, v28, s[16:19], s8 offen nt
	s_waitcnt vmcnt(8)
	v_mov_b32_dpp v108, v32 wave_shr:1 row_mask:0xf bank_mask:0xf bound_ctrl:1
	v_mov_b32_dpp v109, v33 wave_shr:1 row_mask:0xf bank_mask:0xf bound_ctrl:1
	v_mov_b32_dpp v110, v34 wave_shr:1 row_mask:0xf bank_mask:0xf bound_ctrl:1
	v_mov_b32_dpp v112, v32 wave_shl:1 row_mask:0xf bank_mask:0xf bound_ctrl:1
	v_mov_b32_dpp v113, v33 wave_shl:1 row_mask:0xf bank_mask:0xf bound_ctrl:1
	v_mov_b32_dpp v114, v34 wave_shl:1 row_mask:0xf bank_mask:0xf bound_ctrl:1
	s_add_i32 s4, s34, 1
	s_cmpk_lt_u32 s4, 0x201
	s_cselect_b64 s[12:13], s[40:41], 0
	v_cmp_eq_u32_e64 s[14:15], s37, v31
	s_and_b64 s[14:15], s[14:15], s[12:13]
	v_cndmask_b32_e64 v29, 0, 1, s[14:15]
	v_mul_f32_e64 v80, v32, v32
	v_mul_f32_e64 v81, v32, v33
	v_mul_f32_e64 v102, v32, v34
	v_mul_f32_e64 v103, v33, v33
	v_mul_f32_e64 v116, v33, v34
	v_mul_f32_e64 v117, v34, v34
	v_or_b32_dpp v53, v29, v29 wave_shr:1 row_mask:0xf bank_mask:0xf bound_ctrl:1
	s_nop 1
	v_or_b32_dpp v53, v29, v53 wave_shl:1 row_mask:0xf bank_mask:0xf bound_ctrl:1
	s_nop 1
	v_or_b32_dpp v84, v53, v53 wave_shr:1 row_mask:0xf bank_mask:0xf bound_ctrl:1
	s_nop 1
	v_or_b32_dpp v84, v53, v84 wave_shl:1 row_mask:0xf bank_mask:0xf bound_ctrl:1
	v_or3_b32 v29, v84, v85, v52
	v_or3_b32 v29, v29, v30, v25
	s_add_i32 s4, s34, -2
	s_cmpk_lt_u32 s4, 0x1ff
	s_cselect_b64 s[12:13], s[42:43], 0
	v_cmp_ne_u32_e64 s[30:31], 0, v29
	s_and_b64 s[30:31], s[30:31], s[12:13]
	v_cndmask_b32_e64 v29, 0, 1.0, s[30:31]
	v_add_f32_e64 v118, v32, v108
	v_add_f32_e64 v119, v33, v109
	v_add_f32_e64 v120, v34, v110
	v_fma_f32 v80, v108, v108, v80
	v_fma_f32 v81, v108, v109, v81
	v_fma_f32 v102, v108, v110, v102
	v_fma_f32 v103, v109, v109, v103
	v_fma_f32 v116, v109, v110, v116
	v_fma_f32 v117, v110, v110, v117
	v_add_f32_dpp v127, v29, v29 wave_shr:1 row_mask:0xf bank_mask:0xf bound_ctrl:1
	v_add_f32_e64 v118, v118, v112
	v_add_f32_e64 v119, v119, v113
	v_add_f32_e64 v120, v120, v114
	v_fma_f32 v121, v112, v112, v80
	v_fma_f32 v122, v112, v113, v81
	v_fma_f32 v123, v112, v114, v102
	v_fma_f32 v124, v113, v113, v103
	v_fma_f32 v125, v113, v114, v116
	v_fma_f32 v126, v114, v114, v117
	v_add_f32_dpp v127, v29, v127 wave_shl:1 row_mask:0xf bank_mask:0xf bound_ctrl:1
	v_pk_add_f32 v[80:81], v[86:87], v[118:119]
	v_pk_add_f32 v[102:103], v[44:45], v[80:81]
	v_pk_add_f32 v[44:45], v[88:89], v[120:121]
	v_pk_add_f32 v[86:87], v[54:55], v[44:45]
	v_pk_add_f32 v[54:55], v[90:91], v[122:123]
	v_pk_add_f32 v[88:89], v[56:57], v[54:55]
	v_pk_add_f32 v[56:57], v[92:93], v[124:125]
	v_pk_add_f32 v[90:91], v[58:59], v[56:57]
	v_pk_add_f32 v[58:59], v[94:95], v[126:127]
	v_pk_add_f32 v[92:93], v[60:61], v[58:59]
	v_mul_f32_e64 v128, v102, v22
	v_mul_f32_e64 v129, v103, v22
	v_mul_f32_e64 v130, v86, v22
	v_fma_f32 v29, v87, v22, v26
	v_mul_f32_e64 v53, v88, v22
	v_mul_f32_e64 v60, v89, v22
	v_fma_f32 v61, v90, v22, v26
	v_mul_f32_e64 v94, v91, v22
	v_fma_f32 v95, v92, v22, v26
	v_fma_f32 v29, -v128, v128, v29
	v_fma_f32 v53, -v128, v129, v53
	v_fma_f32 v60, -v128, v130, v60
	v_fma_f32 v61, -v129, v129, v61
	v_fma_f32 v94, -v129, v130, v94
	v_fma_f32 v95, -v130, v130, v95
	v_mul_f32_e64 v116, v94, v94
	v_mul_f32_e64 v117, v53, v95
	v_mul_f32_e64 v140, v60, v61
	v_mul_f32_e64 v141, v60, v60
	v_mul_f32_e64 v142, v29, v94
	v_mul_f32_e64 v143, v53, v53
	v_fma_f32 v116, v61, v95, -v116
	v_fma_f32 v117, v60, v94, -v117
	v_fma_f32 v140, v53, v94, -v140
	v_fma_f32 v141, v29, v95, -v141
	v_fma_f32 v142, v53, v60, -v142
	v_fma_f32 v143, v29, v61, -v143
	v_mul_f32_e64 v144, v29, v116
	v_fma_f32 v144, v53, v117, v144
	v_fma_f32 v144, v60, v140, v144
	v_rcp_f32_e32 v144, v144
	v_cmp_ne_u32_e64 vcc, s37, v2
	v_mul_f32_e64 v144, v144, v22
	v_cndmask_b32_e64 v144, 0, v144, s[30:31]
	v_cndmask_b32_e64 v29, 0, v18, vcc
	v_cndmask_b32_e64 v137, 0, v22, s[30:31]
	v_mul_f32_e64 v131, v116, v144
	v_mul_f32_e64 v132, v117, v144
	v_mul_f32_e64 v133, v140, v144
	v_mul_f32_e64 v134, v141, v144
	v_mul_f32_e64 v135, v142, v144
	v_mul_f32_e64 v136, v143, v144
	v_add_f32_e64 v138, v93, v29
	v_mov_b32_e32 v139, v2
	ds_write_b128 v23, v[128:131]
	ds_write_b128 v23, v[132:135] offset:1024
	ds_write_b128 v23, v[136:139] offset:2048
	s_waitcnt lgkmcnt(0)
	s_barrier
	v_mov_b32_dpp v60, v20 wave_shr:1 row_mask:0xf bank_mask:0xf bound_ctrl:1
	v_mov_b32_dpp v61, v21 wave_shr:1 row_mask:0xf bank_mask:0xf bound_ctrl:1
	v_mov_b32_dpp v86, v20 wave_shl:1 row_mask:0xf bank_mask:0xf bound_ctrl:1
	v_mov_b32_dpp v87, v21 wave_shl:1 row_mask:0xf bank_mask:0xf bound_ctrl:1
	v_pk_mul_f32 v[88:89], v[20:21], v[32:33] op_sel_hi:[1,0]
	v_pk_mul_f32 v[90:91], v[20:21], v[32:33] op_sel:[0,1]
	v_pk_mul_f32 v[92:93], v[20:21], v[34:35] op_sel_hi:[1,0]
	v_pk_add_f32 v[94:95], v[20:21], v[60:61]
	v_pk_fma_f32 v[88:89], v[60:61], v[108:109], v[88:89] op_sel_hi:[1,0,1]
	v_pk_fma_f32 v[90:91], v[60:61], v[108:109], v[90:91] op_sel:[0,1,0]
	v_pk_fma_f32 v[92:93], v[60:61], v[110:111], v[92:93] op_sel_hi:[1,0,1]
	v_pk_add_f32 v[94:95], v[94:95], v[86:87]
	v_pk_fma_f32 v[88:89], v[86:87], v[112:113], v[88:89] op_sel_hi:[1,0,1]
	v_pk_fma_f32 v[90:91], v[86:87], v[112:113], v[90:91] op_sel:[0,1,0]
	v_pk_fma_f32 v[92:93], v[86:87], v[114:115], v[92:93] op_sel_hi:[1,0,1]
	v_pk_add_f32 v[60:61], v[100:101], v[94:95]
	v_pk_add_f32 v[86:87], v[66:67], v[60:61]
	v_pk_add_f32 v[66:67], v[82:83], v[88:89]
	v_pk_add_f32 v[100:101], v[50:51], v[66:67]
	v_pk_add_f32 v[50:51], v[96:97], v[90:91]
	v_pk_add_f32 v[82:83], v[62:63], v[50:51]
	v_pk_add_f32 v[62:63], v[98:99], v[92:93]
	v_pk_add_f32 v[96:97], v[64:65], v[62:63]
	v_pk_fma_f32 v[100:101], v[128:129], v[86:87], v[100:101] op_sel_hi:[0,1,1] neg_lo:[1,0,0] neg_hi:[1,0,0]
	v_pk_fma_f32 v[82:83], v[128:129], v[86:87], v[82:83] op_sel:[1,0,0] neg_lo:[1,0,0] neg_hi:[1,0,0]
	v_pk_fma_f32 v[96:97], v[130:131], v[86:87], v[96:97] op_sel_hi:[0,1,1] neg_lo:[1,0,0] neg_hi:[1,0,0]
	v_pk_mul_f32 v[64:65], v[130:131], v[100:101] op_sel:[1,0]
	v_pk_mul_f32 v[98:99], v[132:133], v[100:101] op_sel_hi:[0,1]
	v_pk_mul_f32 v[102:103], v[132:133], v[100:101] op_sel:[1,0]
	v_pk_fma_f32 v[64:65], v[132:133], v[82:83], v[64:65] op_sel_hi:[0,1,1]
	v_pk_fma_f32 v[98:99], v[134:135], v[82:83], v[98:99] op_sel_hi:[0,1,1]
	v_pk_fma_f32 v[102:103], v[134:135], v[82:83], v[102:103] op_sel:[1,0,0]
	v_pk_fma_f32 v[64:65], v[132:133], v[96:97], v[64:65] op_sel:[1,0,0]
	v_pk_fma_f32 v[98:99], v[134:135], v[96:97], v[98:99] op_sel:[1,0,0]
	v_pk_fma_f32 v[102:103], v[136:137], v[96:97], v[102:103] op_sel_hi:[0,1,1]
	v_pk_mul_f32 v[116:117], v[128:129], v[64:65] op_sel_hi:[0,1]
	v_pk_fma_f32 v[116:117], v[128:129], v[98:99], v[116:117] op_sel:[1,0,0]
	v_pk_fma_f32 v[116:117], v[130:131], v[102:103], v[116:117] op_sel_hi:[0,1,1]
	v_pk_fma_f32 v[116:117], v[136:137], v[86:87], v[116:117] op_sel:[1,0,0] neg_lo:[0,0,1] neg_hi:[0,0,1]
	s_add_i32 s5, s34, 3
	s_min_i32 s5, s5, 0x200
	s_mul_i32 s6, s5, 0x804
	s_add_i32 s6, s6, s35
	s_add_i32 s7, s6, 0x505014
	s_add_i32 s8, s6, 0x606018
	s_mul_i32 s9, s5, 0x180c
	s_add_i32 s9, s9, s33
	s_add_i32 s4, s34, 4
	s_min_i32 s4, s4, 0x200
	s_mul_i32 s4, s4, 0x804
	s_add_i32 s4, s4, s38
	buffer_load_dword v2, v28, s[20:23], s4 offen nt
	buffer_load_dwordx3 v[8:10], v27, s[24:27], s9 offen nt
	buffer_load_dword v4, v28, s[16:19], s7 offen nt
	buffer_load_dword v5, v28, s[16:19], s8 offen nt
	s_waitcnt vmcnt(8)
	v_mov_b32_dpp v36, v68 wave_shr:1 row_mask:0xf bank_mask:0xf bound_ctrl:1
	v_mov_b32_dpp v37, v69 wave_shr:1 row_mask:0xf bank_mask:0xf bound_ctrl:1
	v_mov_b32_dpp v38, v70 wave_shr:1 row_mask:0xf bank_mask:0xf bound_ctrl:1
	v_mov_b32_dpp v40, v68 wave_shl:1 row_mask:0xf bank_mask:0xf bound_ctrl:1
	v_mov_b32_dpp v41, v69 wave_shl:1 row_mask:0xf bank_mask:0xf bound_ctrl:1
	v_mov_b32_dpp v42, v70 wave_shl:1 row_mask:0xf bank_mask:0xf bound_ctrl:1
	s_add_i32 s4, s34, 2
	s_cmpk_lt_u32 s4, 0x201
	s_cselect_b64 s[12:13], s[40:41], 0
	v_cmp_eq_u32_e64 s[14:15], s37, v24
	s_and_b64 s[14:15], s[14:15], s[12:13]
	v_cndmask_b32_e64 v25, 0, 1, s[14:15]
	v_mul_f32_e64 v82, v68, v68
	v_mul_f32_e64 v83, v68, v69
	v_mul_f32_e64 v86, v68, v70
	v_mul_f32_e64 v87, v69, v69
	v_mul_f32_e64 v96, v69, v70
	v_mul_f32_e64 v97, v70, v70
	v_or_b32_dpp v29, v25, v25 wave_shr:1 row_mask:0xf bank_mask:0xf bound_ctrl:1
	s_nop 1
	v_or_b32_dpp v29, v25, v29 wave_shl:1 row_mask:0xf bank_mask:0xf bound_ctrl:1
	s_nop 1
	v_or_b32_dpp v53, v29, v29 wave_shr:1 row_mask:0xf bank_mask:0xf bound_ctrl:1
	s_nop 1
	v_or_b32_dpp v53, v29, v53 wave_shl:1 row_mask:0xf bank_mask:0xf bound_ctrl:1
	v_or3_b32 v25, v53, v84, v85
	v_or3_b32 v25, v25, v52, v30
	s_add_i32 s4, s34, -1
	s_cmpk_lt_u32 s4, 0x1ff
	s_cselect_b64 s[12:13], s[42:43], 0
	v_cmp_ne_u32_e64 s[30:31], 0, v25
	s_and_b64 s[30:31], s[30:31], s[12:13]
	v_cndmask_b32_e64 v25, 0, 1.0, s[30:31]
	v_add_f32_e64 v100, v68, v36
	v_add_f32_e64 v101, v69, v37
	v_add_f32_e64 v128, v70, v38
	v_fma_f32 v82, v36, v36, v82
	v_fma_f32 v83, v36, v37, v83
	v_fma_f32 v86, v36, v38, v86
	v_fma_f32 v87, v37, v37, v87
	v_fma_f32 v96, v37, v38, v96
	v_fma_f32 v97, v38, v38, v97
	v_add_f32_dpp v135, v25, v25 wave_shr:1 row_mask:0xf bank_mask:0xf bound_ctrl:1
	v_add_f32_e64 v100, v100, v40
	v_add_f32_e64 v101, v101, v41
	v_add_f32_e64 v128, v128, v42
	v_fma_f32 v129, v40, v40, v82
	v_fma_f32 v130, v40, v41, v83
	v_fma_f32 v131, v40, v42, v86
	v_fma_f32 v132, v41, v41, v87
	v_fma_f32 v133, v41, v42, v96
	v_fma_f32 v134, v42, v42, v97
	v_add_f32_dpp v135, v25, v135 wave_shl:1 row_mask:0xf bank_mask:0xf bound_ctrl:1
	v_pk_add_f32 v[82:83], v[80:81], v[100:101]
	v_pk_add_f32 v[80:81], v[44:45], v[128:129]
	v_pk_add_f32 v[44:45], v[54:55], v[130:131]
	v_pk_add_f32 v[54:55], v[56:57], v[132:133]
	v_pk_add_f32 v[56:57], v[58:59], v[134:135]
	v_mul_f32_e64 v136, v82, v22
	v_mul_f32_e64 v137, v83, v22
	v_mul_f32_e64 v138, v80, v22
	v_fma_f32 v25, v81, v22, v26
	v_mul_f32_e64 v29, v44, v22
	v_mul_f32_e64 v58, v45, v22
	v_fma_f32 v59, v54, v22, v26
	v_mul_f32_e64 v86, v55, v22
	v_fma_f32 v87, v56, v22, v26
	v_fma_f32 v25, -v136, v136, v25
	v_fma_f32 v29, -v136, v137, v29
	v_fma_f32 v58, -v136, v138, v58
	v_fma_f32 v59, -v137, v137, v59
	v_fma_f32 v86, -v137, v138, v86
	v_fma_f32 v87, -v138, v138, v87
	v_mul_f32_e64 v96, v86, v86
	v_mul_f32_e64 v97, v29, v87
	v_mul_f32_e64 v148, v58, v59
	v_mul_f32_e64 v149, v58, v58
	v_mul_f32_e64 v150, v25, v86
	v_mul_f32_e64 v151, v29, v29
	v_fma_f32 v96, v59, v87, -v96
	v_fma_f32 v97, v58, v86, -v97
	v_fma_f32 v148, v29, v86, -v148
	v_fma_f32 v149, v25, v87, -v149
	v_fma_f32 v150, v29, v58, -v150
	v_fma_f32 v151, v25, v59, -v151
	v_mul_f32_e64 v152, v25, v96
	v_fma_f32 v152, v29, v97, v152
	v_fma_f32 v152, v58, v148, v152
	v_rcp_f32_e32 v152, v152
	v_cmp_ne_u32_e64 vcc, s37, v3
	v_mul_f32_e64 v152, v152, v22
	v_cndmask_b32_e64 v152, 0, v152, s[30:31]
	v_cndmask_b32_e64 v25, 0, v18, vcc
	v_cndmask_b32_e64 v145, 0, v22, s[30:31]
	v_mul_f32_e64 v139, v96, v152
	v_mul_f32_e64 v140, v97, v152
	v_mul_f32_e64 v141, v148, v152
	v_mul_f32_e64 v142, v149, v152
	v_mul_f32_e64 v143, v150, v152
	v_mul_f32_e64 v144, v151, v152
	v_add_f32_e64 v146, v57, v25
	v_mov_b32_e32 v147, v3
	ds_write_b128 v23, v[136:139] offset:3072
	ds_write_b128 v23, v[140:143] offset:4096
	ds_write_b128 v23, v[144:147] offset:5120
	s_waitcnt lgkmcnt(0)
	s_barrier
	v_mov_b32_dpp v44, v46 wave_shr:1 row_mask:0xf bank_mask:0xf bound_ctrl:1
	v_mov_b32_dpp v45, v47 wave_shr:1 row_mask:0xf bank_mask:0xf bound_ctrl:1
	v_mov_b32_dpp v54, v46 wave_shl:1 row_mask:0xf bank_mask:0xf bound_ctrl:1
	v_mov_b32_dpp v55, v47 wave_shl:1 row_mask:0xf bank_mask:0xf bound_ctrl:1
	v_pk_mul_f32 v[56:57], v[46:47], v[68:69] op_sel_hi:[1,0]
	v_pk_mul_f32 v[58:59], v[46:47], v[68:69] op_sel:[0,1]
	v_pk_mul_f32 v[80:81], v[46:47], v[70:71] op_sel_hi:[1,0]
	v_pk_add_f32 v[82:83], v[46:47], v[44:45]
	v_pk_fma_f32 v[56:57], v[44:45], v[36:37], v[56:57] op_sel_hi:[1,0,1]
	v_pk_fma_f32 v[58:59], v[44:45], v[36:37], v[58:59] op_sel:[0,1,0]
	v_pk_fma_f32 v[80:81], v[44:45], v[38:39], v[80:81] op_sel_hi:[1,0,1]
	v_pk_add_f32 v[82:83], v[82:83], v[54:55]
	v_pk_fma_f32 v[56:57], v[54:55], v[40:41], v[56:57] op_sel_hi:[1,0,1]
	v_pk_fma_f32 v[58:59], v[54:55], v[40:41], v[58:59] op_sel:[0,1,0]
	v_pk_fma_f32 v[80:81], v[54:55], v[42:43], v[80:81] op_sel_hi:[1,0,1]
	v_pk_add_f32 v[44:45], v[60:61], v[82:83]
	v_pk_add_f32 v[54:55], v[66:67], v[56:57]
	v_pk_add_f32 v[60:61], v[50:51], v[58:59]
	v_pk_add_f32 v[50:51], v[62:63], v[80:81]
	v_pk_fma_f32 v[54:55], v[136:137], v[44:45], v[54:55] op_sel_hi:[0,1,1] neg_lo:[1,0,0] neg_hi:[1,0,0]
	v_pk_fma_f32 v[60:61], v[136:137], v[44:45], v[60:61] op_sel:[1,0,0] neg_lo:[1,0,0] neg_hi:[1,0,0]
	v_pk_fma_f32 v[50:51], v[138:139], v[44:45], v[50:51] op_sel_hi:[0,1,1] neg_lo:[1,0,0] neg_hi:[1,0,0]
	v_pk_mul_f32 v[62:63], v[138:139], v[54:55] op_sel:[1,0]
	v_pk_mul_f32 v[66:67], v[140:141], v[54:55] op_sel_hi:[0,1]
	v_pk_mul_f32 v[86:87], v[140:141], v[54:55] op_sel:[1,0]
	v_pk_fma_f32 v[62:63], v[140:141], v[60:61], v[62:63] op_sel_hi:[0,1,1]
	v_pk_fma_f32 v[66:67], v[142:143], v[60:61], v[66:67] op_sel_hi:[0,1,1]
	v_pk_fma_f32 v[86:87], v[142:143], v[60:61], v[86:87] op_sel:[1,0,0]
	v_pk_fma_f32 v[62:63], v[140:141], v[50:51], v[62:63] op_sel:[1,0,0]
	v_pk_fma_f32 v[66:67], v[142:143], v[50:51], v[66:67] op_sel:[1,0,0]
	v_pk_fma_f32 v[86:87], v[144:145], v[50:51], v[86:87] op_sel_hi:[0,1,1]
	v_pk_mul_f32 v[96:97], v[136:137], v[62:63] op_sel_hi:[0,1]
	v_pk_fma_f32 v[96:97], v[136:137], v[66:67], v[96:97] op_sel:[1,0,0]
	v_pk_fma_f32 v[96:97], v[138:139], v[86:87], v[96:97] op_sel_hi:[0,1,1]
	v_pk_fma_f32 v[96:97], v[144:145], v[44:45], v[96:97] op_sel:[1,0,0] neg_lo:[0,0,1] neg_hi:[0,0,1]
	s_add_i32 s5, s34, 4
	s_min_i32 s5, s5, 0x200
	s_mul_i32 s6, s5, 0x804
	s_add_i32 s6, s6, s35
	s_add_i32 s7, s6, 0x505014
	s_add_i32 s8, s6, 0x606018
	s_mul_i32 s9, s5, 0x180c
	s_add_i32 s9, s9, s33
	s_add_i32 s4, s34, 5
	s_min_i32 s4, s4, 0x200
	s_mul_i32 s4, s4, 0x804
	s_add_i32 s4, s4, s38
	buffer_load_dword v3, v28, s[20:23], s4 offen nt
	buffer_load_dwordx3 v[12:14], v27, s[24:27], s9 offen nt
	buffer_load_dword v6, v28, s[16:19], s7 offen nt
	buffer_load_dword v7, v28, s[16:19], s8 offen nt
	s_waitcnt vmcnt(8)
	v_mov_b32_dpp v72, v104 wave_shr:1 row_mask:0xf bank_mask:0xf bound_ctrl:1
	v_mov_b32_dpp v73, v105 wave_shr:1 row_mask:0xf bank_mask:0xf bound_ctrl:1
	v_mov_b32_dpp v74, v106 wave_shr:1 row_mask:0xf bank_mask:0xf bound_ctrl:1
	v_mov_b32_dpp v76, v104 wave_shl:1 row_mask:0xf bank_mask:0xf bound_ctrl:1
	v_mov_b32_dpp v77, v105 wave_shl:1 row_mask:0xf bank_mask:0xf bound_ctrl:1
	v_mov_b32_dpp v78, v106 wave_shl:1 row_mask:0xf bank_mask:0xf bound_ctrl:1
	s_add_i32 s4, s34, 3
	s_cmpk_lt_u32 s4, 0x201
	s_cselect_b64 s[12:13], s[40:41], 0
	v_cmp_eq_u32_e64 s[14:15], s37, v17
	s_and_b64 s[14:15], s[14:15], s[12:13]
	v_cndmask_b32_e64 v25, 0, 1, s[14:15]
	v_mul_f32_e64 v44, v104, v104
	v_mul_f32_e64 v45, v104, v105
	v_mul_f32_e64 v50, v104, v106
	v_mul_f32_e64 v51, v105, v105
	v_mul_f32_e64 v54, v105, v106
	v_mul_f32_e64 v55, v106, v106
	v_or_b32_dpp v29, v25, v25 wave_shr:1 row_mask:0xf bank_mask:0xf bound_ctrl:1
	s_nop 1
	v_or_b32_dpp v29, v25, v29 wave_shl:1 row_mask:0xf bank_mask:0xf bound_ctrl:1
	s_nop 1
	v_or_b32_dpp v30, v29, v29 wave_shr:1 row_mask:0xf bank_mask:0xf bound_ctrl:1
	s_nop 1
	v_or_b32_dpp v30, v29, v30 wave_shl:1 row_mask:0xf bank_mask:0xf bound_ctrl:1
	v_or3_b32 v25, v30, v53, v84
	v_or3_b32 v25, v25, v85, v52
	s_add_i32 s4, s34, 0
	s_cmpk_lt_u32 s4, 0x1ff
	s_cselect_b64 s[12:13], s[42:43], 0
	v_cmp_ne_u32_e64 s[30:31], 0, v25
	s_and_b64 s[30:31], s[30:31], s[12:13]
	v_cndmask_b32_e64 v25, 0, 1.0, s[30:31]
	v_add_f32_e64 v60, v104, v72
	v_add_f32_e64 v61, v105, v73
	v_add_f32_e64 v136, v106, v74
	v_fma_f32 v44, v72, v72, v44
	v_fma_f32 v45, v72, v73, v45
	v_fma_f32 v50, v72, v74, v50
	v_fma_f32 v51, v73, v73, v51
	v_fma_f32 v54, v73, v74, v54
	v_fma_f32 v55, v74, v74, v55
	v_add_f32_dpp v143, v25, v25 wave_shr:1 row_mask:0xf bank_mask:0xf bound_ctrl:1
	v_add_f32_e64 v60, v60, v76
	v_add_f32_e64 v61, v61, v77
	v_add_f32_e64 v136, v136, v78
	v_fma_f32 v137, v76, v76, v44
	v_fma_f32 v138, v76, v77, v45
	v_fma_f32 v139, v76, v78, v50
	v_fma_f32 v140, v77, v77, v51
	v_fma_f32 v141, v77, v78, v54
	v_fma_f32 v142, v78, v78, v55
	v_add_f32_dpp v143, v25, v143 wave_shl:1 row_mask:0xf bank_mask:0xf bound_ctrl:1
	v_pk_add_f32 v[44:45], v[100:101], v[60:61]
	v_pk_add_f32 v[50:51], v[118:119], v[44:45]
	v_pk_add_f32 v[54:55], v[128:129], v[136:137]
	v_pk_add_f32 v[100:101], v[120:121], v[54:55]
	v_pk_add_f32 v[118:119], v[130:131], v[138:139]
	v_pk_add_f32 v[120:121], v[122:123], v[118:119]
	v_pk_add_f32 v[122:123], v[132:133], v[140:141]
	v_pk_add_f32 v[128:129], v[124:125], v[122:123]
	v_pk_add_f32 v[124:125], v[134:135], v[142:143]
	v_pk_add_f32 v[130:131], v[126:127], v[124:125]
	v_mul_f32_e64 v132, v50, v22
	v_mul_f32_e64 v133, v51, v22
	v_mul_f32_e64 v134, v100, v22
	v_fma_f32 v25, v101, v22, v26
	v_mul_f32_e64 v29, v120, v22
	v_mul_f32_e64 v126, v121, v22
	v_fma_f32 v127, v128, v22, v26
	v_mul_f32_e64 v152, v129, v22
	v_fma_f32 v153, v130, v22, v26
	v_fma_f32 v25, -v132, v132, v25
	v_fma_f32 v29, -v132, v133, v29
	v_fma_f32 v126, -v132, v134, v126
	v_fma_f32 v127, -v133, v133, v127
	v_fma_f32 v152, -v133, v134, v152
	v_fma_f32 v153, -v134, v134, v153
	v_mul_f32_e64 v154, v152, v152
	v_mul_f32_e64 v155, v29, v153
	v_mul_f32_e64 v156, v126, v127
	v_mul_f32_e64 v157, v126, v126
	v_mul_f32_e64 v158, v25, v152
	v_mul_f32_e64 v159, v29, v29
	v_fma_f32 v154, v127, v153, -v154
	v_fma_f32 v155, v126, v152, -v155
	v_fma_f32 v156, v29, v152, -v156
	v_fma_f32 v157, v25, v153, -v157
	v_fma_f32 v158, v29, v126, -v158
	v_fma_f32 v159, v25, v127, -v159
	v_mul_f32_e64 v160, v25, v154
	v_fma_f32 v160, v29, v155, v160
	v_fma_f32 v160, v126, v156, v160
	v_rcp_f32_e32 v160, v160
	v_cmp_ne_u32_e64 vcc, s37, v16
	v_mul_f32_e64 v160, v160, v22
	v_cndmask_b32_e64 v160, 0, v160, s[30:31]
	v_cndmask_b32_e64 v25, 0, v18, vcc
	v_cndmask_b32_e64 v149, 0, v22, s[30:31]
	v_mul_f32_e64 v135, v154, v160
	v_mul_f32_e64 v144, v155, v160
	v_mul_f32_e64 v145, v156, v160
	v_mul_f32_e64 v146, v157, v160
	v_mul_f32_e64 v147, v158, v160
	v_mul_f32_e64 v148, v159, v160
	v_add_f32_e64 v150, v131, v25
	v_mov_b32_e32 v151, v16
	ds_write_b128 v23, v[132:135]
	ds_write_b128 v23, v[144:147] offset:1024
	ds_write_b128 v23, v[148:151] offset:2048
	s_waitcnt lgkmcnt(0)
	s_barrier
	v_mov_b32_dpp v50, v48 wave_shr:1 row_mask:0xf bank_mask:0xf bound_ctrl:1
	v_mov_b32_dpp v51, v49 wave_shr:1 row_mask:0xf bank_mask:0xf bound_ctrl:1
	v_mov_b32_dpp v100, v48 wave_shl:1 row_mask:0xf bank_mask:0xf bound_ctrl:1
	v_mov_b32_dpp v101, v49 wave_shl:1 row_mask:0xf bank_mask:0xf bound_ctrl:1
	v_pk_mul_f32 v[120:121], v[48:49], v[104:105] op_sel_hi:[1,0]
	v_pk_mul_f32 v[126:127], v[48:49], v[104:105] op_sel:[0,1]
	v_pk_mul_f32 v[128:129], v[48:49], v[106:107] op_sel_hi:[1,0]
	v_pk_add_f32 v[130:131], v[48:49], v[50:51]
	v_pk_fma_f32 v[120:121], v[50:51], v[72:73], v[120:121] op_sel_hi:[1,0,1]
	v_pk_fma_f32 v[126:127], v[50:51], v[72:73], v[126:127] op_sel:[0,1,0]
	v_pk_fma_f32 v[128:129], v[50:51], v[74:75], v[128:129] op_sel_hi:[1,0,1]
	v_pk_add_f32 v[130:131], v[130:131], v[100:101]
	v_pk_fma_f32 v[120:121], v[100:101], v[76:77], v[120:121] op_sel_hi:[1,0,1]
	v_pk_fma_f32 v[126:127], v[100:101], v[76:77], v[126:127] op_sel:[0,1,0]
	v_pk_fma_f32 v[128:129], v[100:101], v[78:79], v[128:129] op_sel_hi:[1,0,1]
	v_pk_add_f32 v[50:51], v[82:83], v[130:131]
	v_pk_add_f32 v[100:101], v[94:95], v[50:51]
	v_pk_add_f32 v[82:83], v[56:57], v[120:121]
	v_pk_add_f32 v[94:95], v[88:89], v[82:83]
	v_pk_add_f32 v[56:57], v[58:59], v[126:127]
	v_pk_add_f32 v[88:89], v[90:91], v[56:57]
	v_pk_add_f32 v[58:59], v[80:81], v[128:129]
	v_pk_add_f32 v[90:91], v[92:93], v[58:59]
	v_pk_fma_f32 v[94:95], v[132:133], v[100:101], v[94:95] op_sel_hi:[0,1,1] neg_lo:[1,0,0] neg_hi:[1,0,0]
	v_pk_fma_f32 v[88:89], v[132:133], v[100:101], v[88:89] op_sel:[1,0,0] neg_lo:[1,0,0] neg_hi:[1,0,0]
	v_pk_fma_f32 v[90:91], v[134:135], v[100:101], v[90:91] op_sel_hi:[0,1,1] neg_lo:[1,0,0] neg_hi:[1,0,0]
	v_pk_mul_f32 v[80:81], v[134:135], v[94:95] op_sel:[1,0]
	v_pk_mul_f32 v[92:93], v[144:145], v[94:95] op_sel_hi:[0,1]
	v_pk_mul_f32 v[152:153], v[144:145], v[94:95] op_sel:[1,0]
	v_pk_fma_f32 v[80:81], v[144:145], v[88:89], v[80:81] op_sel_hi:[0,1,1]
	v_pk_fma_f32 v[92:93], v[146:147], v[88:89], v[92:93] op_sel_hi:[0,1,1]
	v_pk_fma_f32 v[152:153], v[146:147], v[88:89], v[152:153] op_sel:[1,0,0]
	v_pk_fma_f32 v[80:81], v[144:145], v[90:91], v[80:81] op_sel:[1,0,0]
	v_pk_fma_f32 v[92:93], v[146:147], v[90:91], v[92:93] op_sel:[1,0,0]
	v_pk_fma_f32 v[152:153], v[148:149], v[90:91], v[152:153] op_sel_hi:[0,1,1]
	v_pk_mul_f32 v[154:155], v[132:133], v[80:81] op_sel_hi:[0,1]
	v_pk_fma_f32 v[154:155], v[132:133], v[92:93], v[154:155] op_sel:[1,0,0]
	v_pk_fma_f32 v[154:155], v[134:135], v[152:153], v[154:155] op_sel_hi:[0,1,1]
	v_pk_fma_f32 v[154:155], v[148:149], v[100:101], v[154:155] op_sel:[1,0,0] neg_lo:[0,0,1] neg_hi:[0,0,1]
	v_cmp_eq_u32_e64 s[10:11], 6, v151
	v_cmp_eq_u32_e64 s[14:15], 7, v151
	v_pk_add_f32 v[88:89], v[62:63], v[80:81]
	v_pk_add_f32 v[90:91], v[64:65], v[88:89]
	v_pk_add_f32 v[62:63], v[66:67], v[92:93]
	v_pk_add_f32 v[64:65], v[98:99], v[62:63]
	v_pk_add_f32 v[66:67], v[86:87], v[152:153]
	v_pk_add_f32 v[94:95], v[102:103], v[66:67]
	v_pk_add_f32 v[86:87], v[96:97], v[154:155]
	v_pk_add_f32 v[98:99], v[116:117], v[86:87]
	v_pk_fma_f32 v[96:97], v[108:109], v[90:91], v[98:99] op_sel_hi:[0,1,1]
	v_pk_fma_f32 v[100:101], v[112:113], v[90:91], v[98:99] op_sel_hi:[0,1,1]
	v_pk_fma_f32 v[96:97], v[108:109], v[64:65], v[96:97] op_sel:[1,0,0]
	v_pk_fma_f32 v[100:101], v[112:113], v[64:65], v[100:101] op_sel:[1,0,0]
	v_pk_fma_f32 v[96:97], v[110:111], v[94:95], v[96:97] op_sel_hi:[0,1,1]
	v_pk_fma_f32 v[100:101], v[114:115], v[94:95], v[100:101] op_sel_hi:[0,1,1]
	v_pk_fma_f32 v[98:99], v[32:33], v[90:91], v[98:99] op_sel_hi:[0,1,1]
	v_pk_fma_f32 v[98:99], v[32:33], v[64:65], v[98:99] op_sel:[1,0,0]
	v_pk_fma_f32 v[98:99], v[34:35], v[94:95], v[98:99] op_sel_hi:[0,1,1]
	v_cndmask_b32_e64 v102, 0, v18, s[10:11]
	v_cndmask_b32_e64 v103, 0, v18, s[14:15]
	v_add_f32_dpp v98, v96, v98 wave_shl:1 row_mask:0xf bank_mask:0xf bound_ctrl:1
	v_add_f32_dpp v99, v97, v99 wave_shl:1 row_mask:0xf bank_mask:0xf bound_ctrl:1
	s_add_i32 s4, s34, 0
	s_cmpk_lt_i32 s4, 0x201
	s_cselect_b64 s[12:13], s[0:1], 0
	v_add_f32_dpp v98, v100, v98 wave_shr:1 row_mask:0xf bank_mask:0xf bound_ctrl:1
	v_add_f32_dpp v99, v101, v99 wave_shr:1 row_mask:0xf bank_mask:0xf bound_ctrl:1
	v_pk_fma_f32 v[98:99], v[20:21], v[150:151], v[98:99] op_sel_hi:[1,0,1] neg_lo:[0,0,1] neg_hi:[0,0,1]
	v_pk_add_f32 v[98:99], v[98:99], v[102:103] neg_lo:[0,1] neg_hi:[0,1]
	v_pk_mul_f32 v[116:117], v[98:99], v[98:99]
	v_add_f32_e32 v116, v116, v117
	v_cndmask_b32_e64 v117, 0, v116, s[12:13]
	v_add_f32_e32 v1, v1, v117
	s_add_i32 s5, s34, 5
	s_min_i32 s5, s5, 0x200
	s_mul_i32 s6, s5, 0x804
	s_add_i32 s6, s6, s35
	s_add_i32 s7, s6, 0x505014
	s_add_i32 s8, s6, 0x606018
	s_mul_i32 s9, s5, 0x180c
	s_add_i32 s9, s9, s33
	s_add_i32 s4, s34, 6
	s_min_i32 s4, s4, 0x200
	s_mul_i32 s4, s4, 0x804
	s_add_i32 s4, s4, s38
	buffer_load_dword v16, v28, s[20:23], s4 offen nt
	buffer_load_dwordx3 v[32:34], v27, s[24:27], s9 offen nt
	buffer_load_dword v20, v28, s[16:19], s7 offen nt
	buffer_load_dword v21, v28, s[16:19], s8 offen nt
	s_waitcnt vmcnt(8)
	v_mov_b32_dpp v96, v8 wave_shr:1 row_mask:0xf bank_mask:0xf bound_ctrl:1
	v_mov_b32_dpp v97, v9 wave_shr:1 row_mask:0xf bank_mask:0xf bound_ctrl:1
	v_mov_b32_dpp v98, v10 wave_shr:1 row_mask:0xf bank_mask:0xf bound_ctrl:1
	v_mov_b32_dpp v100, v8 wave_shl:1 row_mask:0xf bank_mask:0xf bound_ctrl:1
	v_mov_b32_dpp v101, v9 wave_shl:1 row_mask:0xf bank_mask:0xf bound_ctrl:1
	v_mov_b32_dpp v102, v10 wave_shl:1 row_mask:0xf bank_mask:0xf bound_ctrl:1
	s_add_i32 s4, s34, 4
	s_cmpk_lt_u32 s4, 0x201
	s_cselect_b64 s[12:13], s[40:41], 0
	v_cmp_eq_u32_e64 s[14:15], s37, v2
	s_and_b64 s[14:15], s[14:15], s[12:13]
	v_cndmask_b32_e64 v25, 0, 1, s[14:15]
	v_mul_f32_e64 v64, v8, v8
	v_mul_f32_e64 v65, v8, v9
	v_mul_f32_e64 v90, v8, v10
	v_mul_f32_e64 v91, v9, v9
	v_mul_f32_e64 v94, v9, v10
	v_mul_f32_e64 v95, v10, v10
	v_or_b32_dpp v29, v25, v25 wave_shr:1 row_mask:0xf bank_mask:0xf bound_ctrl:1
	s_nop 1
	v_or_b32_dpp v29, v25, v29 wave_shl:1 row_mask:0xf bank_mask:0xf bound_ctrl:1
	s_nop 1
	v_or_b32_dpp v52, v29, v29 wave_shr:1 row_mask:0xf bank_mask:0xf bound_ctrl:1
	s_nop 1
	v_or_b32_dpp v52, v29, v52 wave_shl:1 row_mask:0xf bank_mask:0xf bound_ctrl:1
	v_or3_b32 v25, v52, v30, v53
	v_or3_b32 v25, v25, v84, v85
	s_add_i32 s4, s34, 1
	s_cmpk_lt_u32 s4, 0x1ff
	s_cselect_b64 s[12:13], s[42:43], 0
	v_cmp_ne_u32_e64 s[30:31], 0, v25
	s_and_b64 s[30:31], s[30:31], s[12:13]
	v_cndmask_b32_e64 v25, 0, 1.0, s[30:31]
	v_add_f32_e64 v108, v8, v96
	v_add_f32_e64 v109, v9, v97
	v_add_f32_e64 v110, v10, v98
	v_fma_f32 v64, v96, v96, v64
	v_fma_f32 v65, v96, v97, v65
	v_fma_f32 v90, v96, v98, v90
	v_fma_f32 v91, v97, v97, v91
	v_fma_f32 v94, v97, v98, v94
	v_fma_f32 v95, v98, v98, v95
	v_add_f32_dpp v117, v25, v25 wave_shr:1 row_mask:0xf bank_mask:0xf bound_ctrl:1
	v_add_f32_e64 v108, v108, v100
	v_add_f32_e64 v109, v109, v101
	v_add_f32_e64 v110, v110, v102
	v_fma_f32 v111, v100, v100, v64
	v_fma_f32 v112, v100, v101, v65
	v_fma_f32 v113, v100, v102, v90
	v_fma_f32 v114, v101, v101, v91
	v_fma_f32 v115, v101, v102, v94
	v_fma_f32 v116, v102, v102, v95
	v_add_f32_dpp v117, v25, v117 wave_shl:1 row_mask:0xf bank_mask:0xf bound_ctrl:1
	v_pk_add_f32 v[64:65], v[44:45], v[108:109]
	v_pk_add_f32 v[44:45], v[54:55], v[110:111]
	v_pk_add_f32 v[54:55], v[118:119], v[112:113]
	v_pk_add_f32 v[90:91], v[122:123], v[114:115]
	v_pk_add_f32 v[94:95], v[124:125], v[116:117]
	v_mul_f32_e64 v132, v64, v22
	v_mul_f32_e64 v133, v65, v22
	v_mul_f32_e64 v134, v44, v22
	v_fma_f32 v25, v45, v22, v26
	v_mul_f32_e64 v29, v54, v22
	v_mul_f32_e64 v118, v55, v22
	v_fma_f32 v119, v90, v22, v26
	v_mul_f32_e64 v122, v91, v22
	v_fma_f32 v123, v94, v22, v26
	v_fma_f32 v25, -v132, v132, v25
	v_fma_f32 v29, -v132, v133, v29
	v_fma_f32 v118, -v132, v134, v118
	v_fma_f32 v119, -v133, v133, v119
	v_fma_f32 v122, -v133, v134, v122
	v_fma_f32 v123, -v134, v134, v123
	v_mul_f32_e64 v124, v122, v122
	v_mul_f32_e64 v125, v29, v123
	v_mul_f32_e64 v156, v118, v119
	v_mul_f32_e64 v157, v118, v118
	v_mul_f32_e64 v158, v25, v122
	v_mul_f32_e64 v159, v29, v29
	v_fma_f32 v124, v119, v123, -v124
	v_fma_f32 v125, v118, v122, -v125
	v_fma_f32 v156, v29, v122, -v156
	v_fma_f32 v157, v25, v123, -v157
	v_fma_f32 v158, v29, v118, -v158
	v_fma_f32 v159, v25, v119, -v159
	v_mul_f32_e64 v160, v25, v124
	v_fma_f32 v160, v29, v125, v160
	v_fma_f32 v160, v118, v156, v160
	v_rcp_f32_e32 v160, v160
	v_cmp_ne_u32_e64 vcc, s37, v31
	v_mul_f32_e64 v160, v160, v22
	v_cndmask_b32_e64 v160, 0, v160, s[30:31]
	v_cndmask_b32_e64 v25, 0, v18, vcc
	v_cndmask_b32_e64 v149, 0, v22, s[30:31]
	v_mul_f32_e64 v135, v124, v160
	v_mul_f32_e64 v144, v125, v160
	v_mul_f32_e64 v145, v156, v160
	v_mul_f32_e64 v146, v157, v160
	v_mul_f32_e64 v147, v158, v160
	v_mul_f32_e64 v148, v159, v160
	v_add_f32_e64 v150, v95, v25
	v_mov_b32_e32 v151, v31
	ds_write_b128 v23, v[132:135] offset:3072
	ds_write_b128 v23, v[144:147] offset:4096
	ds_write_b128 v23, v[148:151] offset:5120
	s_waitcnt lgkmcnt(0)
	s_barrier
	v_mov_b32_dpp v44, v4 wave_shr:1 row_mask:0xf bank_mask:0xf bound_ctrl:1
	v_mov_b32_dpp v45, v5 wave_shr:1 row_mask:0xf bank_mask:0xf bound_ctrl:1
	v_mov_b32_dpp v54, v4 wave_shl:1 row_mask:0xf bank_mask:0xf bound_ctrl:1
	v_mov_b32_dpp v55, v5 wave_shl:1 row_mask:0xf bank_mask:0xf bound_ctrl:1
	v_pk_mul_f32 v[64:65], v[4:5], v[8:9] op_sel_hi:[1,0]
	v_pk_mul_f32 v[90:91], v[4:5], v[8:9] op_sel:[0,1]
	v_pk_mul_f32 v[94:95], v[4:5], v[10:11] op_sel_hi:[1,0]
	v_pk_add_f32 v[118:119], v[4:5], v[44:45]
	v_pk_fma_f32 v[64:65], v[44:45], v[96:97], v[64:65] op_sel_hi:[1,0,1]
	v_pk_fma_f32 v[90:91], v[44:45], v[96:97], v[90:91] op_sel:[0,1,0]
	v_pk_fma_f32 v[94:95], v[44:45], v[98:99], v[94:95] op_sel_hi:[1,0,1]
	v_pk_add_f32 v[118:119], v[118:119], v[54:55]
	v_pk_fma_f32 v[64:65], v[54:55], v[100:101], v[64:65] op_sel_hi:[1,0,1]
	v_pk_fma_f32 v[90:91], v[54:55], v[100:101], v[90:91] op_sel:[0,1,0]
	v_pk_fma_f32 v[94:95], v[54:55], v[102:103], v[94:95] op_sel_hi:[1,0,1]
	v_pk_add_f32 v[44:45], v[50:51], v[118:119]
	v_pk_add_f32 v[50:51], v[82:83], v[64:65]
	v_pk_add_f32 v[54:55], v[56:57], v[90:91]
	v_pk_add_f32 v[56:57], v[58:59], v[94:95]
	v_pk_fma_f32 v[50:51], v[132:133], v[44:45], v[50:51] op_sel_hi:[0,1,1] neg_lo:[1,0,0] neg_hi:[1,0,0]
	v_pk_fma_f32 v[54:55], v[132:133], v[44:45], v[54:55] op_sel:[1,0,0] neg_lo:[1,0,0] neg_hi:[1,0,0]
	v_pk_fma_f32 v[56:57], v[134:135], v[44:45], v[56:57] op_sel_hi:[0,1,1] neg_lo:[1,0,0] neg_hi:[1,0,0]
	v_pk_mul_f32 v[58:59], v[134:135], v[50:51] op_sel:[1,0]
	v_pk_mul_f32 v[82:83], v[144:145], v[50:51] op_sel_hi:[0,1]
	v_pk_mul_f32 v[122:123], v[144:145], v[50:51] op_sel:[1,0]
	v_pk_fma_f32 v[58:59], v[144:145], v[54:55], v[58:59] op_sel_hi:[0,1,1]
	v_pk_fma_f32 v[82:83], v[146:147], v[54:55], v[82:83] op_sel_hi:[0,1,1]
	v_pk_fma_f32 v[122:123], v[146:147], v[54:55], v[122:123] op_sel:[1,0,0]
	v_pk_fma_f32 v[58:59], v[144:145], v[56:57], v[58:59] op_sel:[1,0,0]
	v_pk_fma_f32 v[82:83], v[146:147], v[56:57], v[82:83] op_sel:[1,0,0]
	v_pk_fma_f32 v[122:123], v[148:149], v[56:57], v[122:123] op_sel_hi:[0,1,1]
	v_pk_mul_f32 v[124:125], v[132:133], v[58:59] op_sel_hi:[0,1]
	v_pk_fma_f32 v[124:125], v[132:133], v[82:83], v[124:125] op_sel:[1,0,0]
	v_pk_fma_f32 v[124:125], v[134:135], v[122:123], v[124:125] op_sel_hi:[0,1,1]
	v_pk_fma_f32 v[124:125], v[148:149], v[44:45], v[124:125] op_sel:[1,0,0] neg_lo:[0,0,1] neg_hi:[0,0,1]
	v_cmp_eq_u32_e64 s[10:11], 6, v151
	v_cmp_eq_u32_e64 s[14:15], 7, v151
	v_pk_add_f32 v[44:45], v[88:89], v[58:59]
	v_pk_add_f32 v[50:51], v[62:63], v[82:83]
	v_pk_add_f32 v[54:55], v[66:67], v[122:123]
	v_pk_add_f32 v[56:57], v[86:87], v[124:125]
	v_pk_fma_f32 v[62:63], v[36:37], v[44:45], v[56:57] op_sel_hi:[0,1,1]
	v_pk_fma_f32 v[66:67], v[40:41], v[44:45], v[56:57] op_sel_hi:[0,1,1]
	v_pk_fma_f32 v[62:63], v[36:37], v[50:51], v[62:63] op_sel:[1,0,0]
	v_pk_fma_f32 v[66:67], v[40:41], v[50:51], v[66:67] op_sel:[1,0,0]
	v_pk_fma_f32 v[62:63], v[38:39], v[54:55], v[62:63] op_sel_hi:[0,1,1]
	v_pk_fma_f32 v[66:67], v[42:43], v[54:55], v[66:67] op_sel_hi:[0,1,1]
	v_pk_fma_f32 v[56:57], v[68:69], v[44:45], v[56:57] op_sel_hi:[0,1,1]
	v_pk_fma_f32 v[56:57], v[68:69], v[50:51], v[56:57] op_sel:[1,0,0]
	v_pk_fma_f32 v[56:57], v[70:71], v[54:55], v[56:57] op_sel_hi:[0,1,1]
	v_cndmask_b32_e64 v86, 0, v18, s[10:11]
	v_cndmask_b32_e64 v87, 0, v18, s[14:15]
	v_add_f32_dpp v56, v62, v56 wave_shl:1 row_mask:0xf bank_mask:0xf bound_ctrl:1
	v_add_f32_dpp v57, v63, v57 wave_shl:1 row_mask:0xf bank_mask:0xf bound_ctrl:1
	s_add_i32 s4, s34, 1
	s_cmpk_lt_i32 s4, 0x201
	s_cselect_b64 s[12:13], s[0:1], 0
	v_add_f32_dpp v56, v66, v56 wave_shr:1 row_mask:0xf bank_mask:0xf bound_ctrl:1
	v_add_f32_dpp v57, v67, v57 wave_shr:1 row_mask:0xf bank_mask:0xf bound_ctrl:1
	v_pk_fma_f32 v[56:57], v[46:47], v[150:151], v[56:57] op_sel_hi:[1,0,1] neg_lo:[0,0,1] neg_hi:[0,0,1]
	v_pk_add_f32 v[56:57], v[56:57], v[86:87] neg_lo:[0,1] neg_hi:[0,1]
	v_pk_mul_f32 v[88:89], v[56:57], v[56:57]
	v_add_f32_e32 v88, v88, v89
	v_cndmask_b32_e64 v89, 0, v88, s[12:13]
	v_add_f32_e32 v1, v1, v89
	s_add_i32 s5, s34, 6
	s_min_i32 s5, s5, 0x200
	s_mul_i32 s6, s5, 0x804
	s_add_i32 s6, s6, s35
	s_add_i32 s7, s6, 0x505014
	s_add_i32 s8, s6, 0x606018
	s_mul_i32 s9, s5, 0x180c
	s_add_i32 s9, s9, s33
	s_add_i32 s4, s34, 7
	s_min_i32 s4, s4, 0x200
	s_mul_i32 s4, s4, 0x804
	s_add_i32 s4, s4, s38
	buffer_load_dword v25, v28, s[20:23], s4 offen nt
	buffer_load_dwordx3 v[40:42], v27, s[24:27], s9 offen nt
	buffer_load_dword v36, v28, s[16:19], s7 offen nt
	buffer_load_dword v37, v28, s[16:19], s8 offen nt
	s_waitcnt vmcnt(8)
	v_mov_b32_dpp v44, v12 wave_shr:1 row_mask:0xf bank_mask:0xf bound_ctrl:1
	v_mov_b32_dpp v45, v13 wave_shr:1 row_mask:0xf bank_mask:0xf bound_ctrl:1
	v_mov_b32_dpp v46, v14 wave_shr:1 row_mask:0xf bank_mask:0xf bound_ctrl:1
	v_mov_b32_dpp v68, v12 wave_shl:1 row_mask:0xf bank_mask:0xf bound_ctrl:1
	v_mov_b32_dpp v69, v13 wave_shl:1 row_mask:0xf bank_mask:0xf bound_ctrl:1
	v_mov_b32_dpp v70, v14 wave_shl:1 row_mask:0xf bank_mask:0xf bound_ctrl:1
	s_add_i32 s4, s34, 5
	s_cmpk_lt_u32 s4, 0x201
	s_cselect_b64 s[12:13], s[40:41], 0
	v_cmp_eq_u32_e64 s[14:15], s37, v3
	s_and_b64 s[14:15], s[14:15], s[12:13]
	v_cndmask_b32_e64 v29, 0, 1, s[14:15]
	v_mul_f32_e64 v38, v12, v12
	v_mul_f32_e64 v39, v12, v13
	v_mul_f32_e64 v50, v12, v14
	v_mul_f32_e64 v51, v13, v13
	v_mul_f32_e64 v54, v13, v14
	v_mul_f32_e64 v55, v14, v14
	v_or_b32_dpp v31, v29, v29 wave_shr:1 row_mask:0xf bank_mask:0xf bound_ctrl:1
	s_nop 1
	v_or_b32_dpp v31, v29, v31 wave_shl:1 row_mask:0xf bank_mask:0xf bound_ctrl:1
	s_nop 1
	v_or_b32_dpp v85, v31, v31 wave_shr:1 row_mask:0xf bank_mask:0xf bound_ctrl:1
	s_nop 1
	v_or_b32_dpp v85, v31, v85 wave_shl:1 row_mask:0xf bank_mask:0xf bound_ctrl:1
	v_or3_b32 v29, v85, v52, v30
	v_or3_b32 v29, v29, v53, v84
	s_add_i32 s4, s34, 2
	s_cmpk_lt_u32 s4, 0x1ff
	s_cselect_b64 s[12:13], s[42:43], 0
	v_cmp_ne_u32_e64 s[30:31], 0, v29
	s_and_b64 s[30:31], s[30:31], s[12:13]
	v_cndmask_b32_e64 v29, 0, 1.0, s[30:31]
	v_add_f32_e64 v56, v12, v44
	v_add_f32_e64 v57, v13, v45
	v_add_f32_e64 v62, v14, v46
	v_fma_f32 v38, v44, v44, v38
	v_fma_f32 v39, v44, v45, v39
	v_fma_f32 v50, v44, v46, v50
	v_fma_f32 v51, v45, v45, v51
	v_fma_f32 v54, v45, v46, v54
	v_fma_f32 v55, v46, v46, v55
	v_add_f32_dpp v89, v29, v29 wave_shr:1 row_mask:0xf bank_mask:0xf bound_ctrl:1
	v_add_f32_e64 v56, v56, v68
	v_add_f32_e64 v57, v57, v69
	v_add_f32_e64 v62, v62, v70
	v_fma_f32 v63, v68, v68, v38
	v_fma_f32 v66, v68, v69, v39
	v_fma_f32 v67, v68, v70, v50
	v_fma_f32 v86, v69, v69, v51
	v_fma_f32 v87, v69, v70, v54
	v_fma_f32 v88, v70, v70, v55
	v_add_f32_dpp v89, v29, v89 wave_shl:1 row_mask:0xf bank_mask:0xf bound_ctrl:1
	v_pk_add_f32 v[38:39], v[108:109], v[56:57]
	v_pk_add_f32 v[50:51], v[60:61], v[38:39]
	v_pk_add_f32 v[54:55], v[110:111], v[62:63]
	v_pk_add_f32 v[60:61], v[136:137], v[54:55]
	v_pk_add_f32 v[108:109], v[112:113], v[66:67]
	v_pk_add_f32 v[110:111], v[138:139], v[108:109]
	v_pk_add_f32 v[112:113], v[114:115], v[86:87]
	v_pk_add_f32 v[132:133], v[140:141], v[112:113]
	v_pk_add_f32 v[114:115], v[116:117], v[88:89]
	v_pk_add_f32 v[134:135], v[142:143], v[114:115]
	v_mul_f32_e64 v136, v50, v22
	v_mul_f32_e64 v137, v51, v22
	v_mul_f32_e64 v138, v60, v22
	v_fma_f32 v29, v61, v22, v26
	v_mul_f32_e64 v31, v110, v22
	v_mul_f32_e64 v116, v111, v22
	v_fma_f32 v117, v132, v22, v26
	v_mul_f32_e64 v148, v133, v22
	v_fma_f32 v149, v134, v22, v26
	v_fma_f32 v29, -v136, v136, v29
	v_fma_f32 v31, -v136, v137, v31
	v_fma_f32 v116, -v136, v138, v116
	v_fma_f32 v117, -v137, v137, v117
	v_fma_f32 v148, -v137, v138, v148
	v_fma_f32 v149, -v138, v138, v149
	v_mul_f32_e64 v150, v148, v148
	v_mul_f32_e64 v151, v31, v149
	v_mul_f32_e64 v156, v116, v117
	v_mul_f32_e64 v157, v116, v116
	v_mul_f32_e64 v158, v29, v148
	v_mul_f32_e64 v159, v31, v31
	v_fma_f32 v150, v117, v149, -v150
	v_fma_f32 v151, v116, v148, -v151
	v_fma_f32 v156, v31, v148, -v156
	v_fma_f32 v157, v29, v149, -v157
	v_fma_f32 v158, v31, v116, -v158
	v_fma_f32 v159, v29, v117, -v159
	v_mul_f32_e64 v160, v29, v150
	v_fma_f32 v160, v31, v151, v160
	v_fma_f32 v160, v116, v156, v160
	v_rcp_f32_e32 v160, v160
	v_cmp_ne_u32_e64 vcc, s37, v24
	v_mul_f32_e64 v160, v160, v22
	v_cndmask_b32_e64 v160, 0, v160, s[30:31]
	v_cndmask_b32_e64 v29, 0, v18, vcc
	v_cndmask_b32_e64 v145, 0, v22, s[30:31]
	v_mul_f32_e64 v139, v150, v160
	v_mul_f32_e64 v140, v151, v160
	v_mul_f32_e64 v141, v156, v160
	v_mul_f32_e64 v142, v157, v160
	v_mul_f32_e64 v143, v158, v160
	v_mul_f32_e64 v144, v159, v160
	v_add_f32_e64 v146, v135, v29
	v_mov_b32_e32 v147, v24
	ds_write_b128 v23, v[136:139]
	ds_write_b128 v23, v[140:143] offset:1024
	ds_write_b128 v23, v[144:147] offset:2048
	s_waitcnt lgkmcnt(0)
	s_barrier
	v_mov_b32_dpp v50, v6 wave_shr:1 row_mask:0xf bank_mask:0xf bound_ctrl:1
	v_mov_b32_dpp v51, v7 wave_shr:1 row_mask:0xf bank_mask:0xf bound_ctrl:1
	v_mov_b32_dpp v60, v6 wave_shl:1 row_mask:0xf bank_mask:0xf bound_ctrl:1
	v_mov_b32_dpp v61, v7 wave_shl:1 row_mask:0xf bank_mask:0xf bound_ctrl:1
	v_pk_mul_f32 v[110:111], v[6:7], v[12:13] op_sel_hi:[1,0]
	v_pk_mul_f32 v[116:117], v[6:7], v[12:13] op_sel:[0,1]
	v_pk_mul_f32 v[132:133], v[6:7], v[14:15] op_sel_hi:[1,0]
	v_pk_add_f32 v[134:135], v[6:7], v[50:51]
	v_pk_fma_f32 v[110:111], v[50:51], v[44:45], v[110:111] op_sel_hi:[1,0,1]
	v_pk_fma_f32 v[116:117], v[50:51], v[44:45], v[116:117] op_sel:[0,1,0]
	v_pk_fma_f32 v[132:133], v[50:51], v[46:47], v[132:133] op_sel_hi:[1,0,1]
	v_pk_add_f32 v[134:135], v[134:135], v[60:61]
	v_pk_fma_f32 v[110:111], v[60:61], v[68:69], v[110:111] op_sel_hi:[1,0,1]
	v_pk_fma_f32 v[116:117], v[60:61], v[68:69], v[116:117] op_sel:[0,1,0]
	v_pk_fma_f32 v[132:133], v[60:61], v[70:71], v[132:133] op_sel_hi:[1,0,1]
	v_pk_add_f32 v[50:51], v[118:119], v[134:135]
	v_pk_add_f32 v[60:61], v[130:131], v[50:51]
	v_pk_add_f32 v[118:119], v[64:65], v[110:111]
	v_pk_add_f32 v[130:131], v[120:121], v[118:119]
	v_pk_add_f32 v[64:65], v[90:91], v[116:117]
	v_pk_add_f32 v[120:121], v[126:127], v[64:65]
	v_pk_add_f32 v[90:91], v[94:95], v[132:133]
	v_pk_add_f32 v[126:127], v[128:129], v[90:91]
	v_pk_fma_f32 v[130:131], v[136:137], v[60:61], v[130:131] op_sel_hi:[0,1,1] neg_lo:[1,0,0] neg_hi:[1,0,0]
	v_pk_fma_f32 v[120:121], v[136:137], v[60:61], v[120:121] op_sel:[1,0,0] neg_lo:[1,0,0] neg_hi:[1,0,0]
	v_pk_fma_f32 v[126:127], v[138:139], v[60:61], v[126:127] op_sel_hi:[0,1,1] neg_lo:[1,0,0] neg_hi:[1,0,0]
	v_pk_mul_f32 v[94:95], v[138:139], v[130:131] op_sel:[1,0]
	v_pk_mul_f32 v[128:129], v[140:141], v[130:131] op_sel_hi:[0,1]
	v_pk_mul_f32 v[148:149], v[140:141], v[130:131] op_sel:[1,0]
	v_pk_fma_f32 v[94:95], v[140:141], v[120:121], v[94:95] op_sel_hi:[0,1,1]
	v_pk_fma_f32 v[128:129], v[142:143], v[120:121], v[128:129] op_sel_hi:[0,1,1]
	v_pk_fma_f32 v[148:149], v[142:143], v[120:121], v[148:149] op_sel:[1,0,0]
	v_pk_fma_f32 v[94:95], v[140:141], v[126:127], v[94:95] op_sel:[1,0,0]
	v_pk_fma_f32 v[128:129], v[142:143], v[126:127], v[128:129] op_sel:[1,0,0]
	v_pk_fma_f32 v[148:149], v[144:145], v[126:127], v[148:149] op_sel_hi:[0,1,1]
	v_pk_mul_f32 v[150:151], v[136:137], v[94:95] op_sel_hi:[0,1]
	v_pk_fma_f32 v[150:151], v[136:137], v[128:129], v[150:151] op_sel:[1,0,0]
	v_pk_fma_f32 v[150:151], v[138:139], v[148:149], v[150:151] op_sel_hi:[0,1,1]
	v_pk_fma_f32 v[150:151], v[144:145], v[60:61], v[150:151] op_sel:[1,0,0] neg_lo:[0,0,1] neg_hi:[0,0,1]
	v_cmp_eq_u32_e64 s[10:11], 6, v147
	v_cmp_eq_u32_e64 s[14:15], 7, v147
	v_pk_add_f32 v[60:61], v[58:59], v[94:95]
	v_pk_add_f32 v[120:121], v[80:81], v[60:61]
	v_pk_add_f32 v[58:59], v[82:83], v[128:129]
	v_pk_add_f32 v[80:81], v[92:93], v[58:59]
	v_pk_add_f32 v[82:83], v[122:123], v[148:149]
	v_pk_add_f32 v[92:93], v[152:153], v[82:83]
	v_pk_add_f32 v[122:123], v[124:125], v[150:151]
	v_pk_add_f32 v[126:127], v[154:155], v[122:123]
	v_pk_fma_f32 v[124:125], v[72:73], v[120:121], v[126:127] op_sel_hi:[0,1,1]
	v_pk_fma_f32 v[130:131], v[76:77], v[120:121], v[126:127] op_sel_hi:[0,1,1]
	v_pk_fma_f32 v[124:125], v[72:73], v[80:81], v[124:125] op_sel:[1,0,0]
	v_pk_fma_f32 v[130:131], v[76:77], v[80:81], v[130:131] op_sel:[1,0,0]
	v_pk_fma_f32 v[124:125], v[74:75], v[92:93], v[124:125] op_sel_hi:[0,1,1]
	v_pk_fma_f32 v[130:131], v[78:79], v[92:93], v[130:131] op_sel_hi:[0,1,1]
	v_pk_fma_f32 v[126:127], v[104:105], v[120:121], v[126:127] op_sel_hi:[0,1,1]
	v_pk_fma_f32 v[126:127], v[104:105], v[80:81], v[126:127] op_sel:[1,0,0]
	v_pk_fma_f32 v[126:127], v[106:107], v[92:93], v[126:127] op_sel_hi:[0,1,1]
	v_cndmask_b32_e64 v152, 0, v18, s[10:11]
	v_cndmask_b32_e64 v153, 0, v18, s[14:15]
	v_add_f32_dpp v126, v124, v126 wave_shl:1 row_mask:0xf bank_mask:0xf bound_ctrl:1
	v_add_f32_dpp v127, v125, v127 wave_shl:1 row_mask:0xf bank_mask:0xf bound_ctrl:1
	s_add_i32 s4, s34, 2
	s_cmpk_lt_i32 s4, 0x201
	s_cselect_b64 s[12:13], s[0:1], 0
	v_add_f32_dpp v126, v130, v126 wave_shr:1 row_mask:0xf bank_mask:0xf bound_ctrl:1
	v_add_f32_dpp v127, v131, v127 wave_shr:1 row_mask:0xf bank_mask:0xf bound_ctrl:1
	v_pk_fma_f32 v[126:127], v[48:49], v[146:147], v[126:127] op_sel_hi:[1,0,1] neg_lo:[0,0,1] neg_hi:[0,0,1]
	v_pk_add_f32 v[126:127], v[126:127], v[152:153] neg_lo:[0,1] neg_hi:[0,1]
	v_pk_mul_f32 v[154:155], v[126:127], v[126:127]
	v_add_f32_e32 v154, v154, v155
	v_cndmask_b32_e64 v155, 0, v154, s[12:13]
	v_add_f32_e32 v1, v1, v155
	s_add_i32 s5, s34, 7
	s_min_i32 s5, s5, 0x200
	s_mul_i32 s6, s5, 0x804
	s_add_i32 s6, s6, s35
	s_add_i32 s7, s6, 0x505014
	s_add_i32 s8, s6, 0x606018
	s_mul_i32 s9, s5, 0x180c
	s_add_i32 s9, s9, s33
	s_add_i32 s4, s34, 8
	s_min_i32 s4, s4, 0x200
	s_mul_i32 s4, s4, 0x804
	s_add_i32 s4, s4, s38
	buffer_load_dword v24, v28, s[20:23], s4 offen nt
	buffer_load_dwordx3 v[72:74], v27, s[24:27], s9 offen nt
	buffer_load_dword v48, v28, s[16:19], s7 offen nt
	buffer_load_dword v49, v28, s[16:19], s8 offen nt
	s_waitcnt vmcnt(8)
	v_mov_b32_dpp v76, v32 wave_shr:1 row_mask:0xf bank_mask:0xf bound_ctrl:1
	v_mov_b32_dpp v77, v33 wave_shr:1 row_mask:0xf bank_mask:0xf bound_ctrl:1
	v_mov_b32_dpp v78, v34 wave_shr:1 row_mask:0xf bank_mask:0xf bound_ctrl:1
	v_mov_b32_dpp v104, v32 wave_shl:1 row_mask:0xf bank_mask:0xf bound_ctrl:1
	v_mov_b32_dpp v105, v33 wave_shl:1 row_mask:0xf bank_mask:0xf bound_ctrl:1
	v_mov_b32_dpp v106, v34 wave_shl:1 row_mask:0xf bank_mask:0xf bound_ctrl:1
	s_add_i32 s4, s34, 6
	s_cmpk_lt_u32 s4, 0x201
	s_cselect_b64 s[12:13], s[40:41], 0
	v_cmp_eq_u32_e64 s[14:15], s37, v16
	s_and_b64 s[14:15], s[14:15], s[12:13]
	v_cndmask_b32_e64 v29, 0, 1, s[14:15]
	v_mul_f32_e64 v80, v32, v32
	v_mul_f32_e64 v81, v32, v33
	v_mul_f32_e64 v92, v32, v34
	v_mul_f32_e64 v93, v33, v33
	v_mul_f32_e64 v120, v33, v34
	v_mul_f32_e64 v121, v34, v34
	v_or_b32_dpp v31, v29, v29 wave_shr:1 row_mask:0xf bank_mask:0xf bound_ctrl:1
	s_nop 1
	v_or_b32_dpp v31, v29, v31 wave_shl:1 row_mask:0xf bank_mask:0xf bound_ctrl:1
	s_nop 1
	v_or_b32_dpp v84, v31, v31 wave_shr:1 row_mask:0xf bank_mask:0xf bound_ctrl:1
	s_nop 1
	v_or_b32_dpp v84, v31, v84 wave_shl:1 row_mask:0xf bank_mask:0xf bound_ctrl:1
	v_or3_b32 v29, v84, v85, v52
	v_or3_b32 v29, v29, v30, v53
	s_add_i32 s4, s34, 3
	s_cmpk_lt_u32 s4, 0x1ff
	s_cselect_b64 s[12:13], s[42:43], 0
	v_cmp_ne_u32_e64 s[30:31], 0, v29
	s_and_b64 s[30:31], s[30:31], s[12:13]
	v_cndmask_b32_e64 v29, 0, 1.0, s[30:31]
	v_add_f32_e64 v124, v32, v76
	v_add_f32_e64 v125, v33, v77
	v_add_f32_e64 v126, v34, v78
	v_fma_f32 v80, v76, v76, v80
	v_fma_f32 v81, v76, v77, v81
	v_fma_f32 v92, v76, v78, v92
	v_fma_f32 v93, v77, v77, v93
	v_fma_f32 v120, v77, v78, v120
	v_fma_f32 v121, v78, v78, v121
	v_add_f32_dpp v139, v29, v29 wave_shr:1 row_mask:0xf bank_mask:0xf bound_ctrl:1
	v_add_f32_e64 v124, v124, v104
	v_add_f32_e64 v125, v125, v105
	v_add_f32_e64 v126, v126, v106
	v_fma_f32 v127, v104, v104, v80
	v_fma_f32 v130, v104, v105, v81
	v_fma_f32 v131, v104, v106, v92
	v_fma_f32 v136, v105, v105, v93
	v_fma_f32 v137, v105, v106, v120
	v_fma_f32 v138, v106, v106, v121
	v_add_f32_dpp v139, v29, v139 wave_shl:1 row_mask:0xf bank_mask:0xf bound_ctrl:1
	v_pk_add_f32 v[80:81], v[38:39], v[124:125]
	v_pk_add_f32 v[38:39], v[54:55], v[126:127]
	v_pk_add_f32 v[54:55], v[108:109], v[130:131]
	v_pk_add_f32 v[92:93], v[112:113], v[136:137]
	v_pk_add_f32 v[108:109], v[114:115], v[138:139]
	v_mul_f32_e64 v112, v80, v22
	v_mul_f32_e64 v113, v81, v22
	v_mul_f32_e64 v114, v38, v22
	v_fma_f32 v29, v39, v22, v26
	v_mul_f32_e64 v31, v54, v22
	v_mul_f32_e64 v120, v55, v22
	v_fma_f32 v121, v92, v22, v26
	v_mul_f32_e64 v152, v93, v22
	v_fma_f32 v153, v108, v22, v26
	v_fma_f32 v29, -v112, v112, v29
	v_fma_f32 v31, -v112, v113, v31
	v_fma_f32 v120, -v112, v114, v120
	v_fma_f32 v121, -v113, v113, v121
	v_fma_f32 v152, -v113, v114, v152
	v_fma_f32 v153, -v114, v114, v153
	v_mul_f32_e64 v154, v152, v152
	v_mul_f32_e64 v155, v31, v153
	v_mul_f32_e64 v156, v120, v121
	v_mul_f32_e64 v157, v120, v120
	v_mul_f32_e64 v158, v29, v152
	v_mul_f32_e64 v159, v31, v31
	v_fma_f32 v154, v121, v153, -v154
	v_fma_f32 v155, v120, v152, -v155
	v_fma_f32 v156, v31, v152, -v156
	v_fma_f32 v157, v29, v153, -v157
	v_fma_f32 v158, v31, v120, -v158
	v_fma_f32 v159, v29, v121, -v159
	v_mul_f32_e64 v160, v29, v154
	v_fma_f32 v160, v31, v155, v160
	v_fma_f32 v160, v120, v156, v160
	v_rcp_f32_e32 v160, v160
	v_cmp_ne_u32_e64 vcc, s37, v17
	v_mul_f32_e64 v160, v160, v22
	v_cndmask_b32_e64 v160, 0, v160, s[30:31]
	v_cndmask_b32_e64 v29, 0, v18, vcc
	v_cndmask_b32_e64 v145, 0, v22, s[30:31]
	v_mul_f32_e64 v115, v154, v160
	v_mul_f32_e64 v140, v155, v160
	v_mul_f32_e64 v141, v156, v160
	v_mul_f32_e64 v142, v157, v160
	v_mul_f32_e64 v143, v158, v160
	v_mul_f32_e64 v144, v159, v160
	v_add_f32_e64 v146, v109, v29
	v_mov_b32_e32 v147, v17
	ds_write_b128 v23, v[112:115] offset:3072
	ds_write_b128 v23, v[140:143] offset:4096
	ds_write_b128 v23, v[144:147] offset:5120
	s_waitcnt lgkmcnt(0)
	s_barrier
	v_mov_b32_dpp v38, v20 wave_shr:1 row_mask:0xf bank_mask:0xf bound_ctrl:1
	v_mov_b32_dpp v39, v21 wave_shr:1 row_mask:0xf bank_mask:0xf bound_ctrl:1
	v_mov_b32_dpp v54, v20 wave_shl:1 row_mask:0xf bank_mask:0xf bound_ctrl:1
	v_mov_b32_dpp v55, v21 wave_shl:1 row_mask:0xf bank_mask:0xf bound_ctrl:1
	v_pk_mul_f32 v[80:81], v[20:21], v[32:33] op_sel_hi:[1,0]
	v_pk_mul_f32 v[92:93], v[20:21], v[32:33] op_sel:[0,1]
	v_pk_mul_f32 v[108:109], v[20:21], v[34:35] op_sel_hi:[1,0]
	v_pk_add_f32 v[120:121], v[20:21], v[38:39]
	v_pk_fma_f32 v[80:81], v[38:39], v[76:77], v[80:81] op_sel_hi:[1,0,1]
	v_pk_fma_f32 v[92:93], v[38:39], v[76:77], v[92:93] op_sel:[0,1,0]
	v_pk_fma_f32 v[108:109], v[38:39], v[78:79], v[108:109] op_sel_hi:[1,0,1]
	v_pk_add_f32 v[120:121], v[120:121], v[54:55]
	v_pk_fma_f32 v[80:81], v[54:55], v[104:105], v[80:81] op_sel_hi:[1,0,1]
	v_pk_fma_f32 v[92:93], v[54:55], v[104:105], v[92:93] op_sel:[0,1,0]
	v_pk_fma_f32 v[108:109], v[54:55], v[106:107], v[108:109] op_sel_hi:[1,0,1]
	v_pk_add_f32 v[38:39], v[50:51], v[120:121]
	v_pk_add_f32 v[50:51], v[118:119], v[80:81]
	v_pk_add_f32 v[54:55], v[64:65], v[92:93]
	v_pk_add_f32 v[64:65], v[90:91], v[108:109]
	v_pk_fma_f32 v[50:51], v[112:113], v[38:39], v[50:51] op_sel_hi:[0,1,1] neg_lo:[1,0,0] neg_hi:[1,0,0]
	v_pk_fma_f32 v[54:55], v[112:113], v[38:39], v[54:55] op_sel:[1,0,0] neg_lo:[1,0,0] neg_hi:[1,0,0]
	v_pk_fma_f32 v[64:65], v[114:115], v[38:39], v[64:65] op_sel_hi:[0,1,1] neg_lo:[1,0,0] neg_hi:[1,0,0]
	v_pk_mul_f32 v[90:91], v[114:115], v[50:51] op_sel:[1,0]
	v_pk_mul_f32 v[118:119], v[140:141], v[50:51] op_sel_hi:[0,1]
	v_pk_mul_f32 v[152:153], v[140:141], v[50:51] op_sel:[1,0]
	v_pk_fma_f32 v[90:91], v[140:141], v[54:55], v[90:91] op_sel_hi:[0,1,1]
	v_pk_fma_f32 v[118:119], v[142:143], v[54:55], v[118:119] op_sel_hi:[0,1,1]
	v_pk_fma_f32 v[152:153], v[142:143], v[54:55], v[152:153] op_sel:[1,0,0]
	v_pk_fma_f32 v[90:91], v[140:141], v[64:65], v[90:91] op_sel:[1,0,0]
	v_pk_fma_f32 v[118:119], v[142:143], v[64:65], v[118:119] op_sel:[1,0,0]
	v_pk_fma_f32 v[152:153], v[144:145], v[64:65], v[152:153] op_sel_hi:[0,1,1]
	v_pk_mul_f32 v[154:155], v[112:113], v[90:91] op_sel_hi:[0,1]
	v_pk_fma_f32 v[154:155], v[112:113], v[118:119], v[154:155] op_sel:[1,0,0]
	v_pk_fma_f32 v[154:155], v[114:115], v[152:153], v[154:155] op_sel_hi:[0,1,1]
	v_pk_fma_f32 v[154:155], v[144:145], v[38:39], v[154:155] op_sel:[1,0,0] neg_lo:[0,0,1] neg_hi:[0,0,1]
	v_cmp_eq_u32_e64 s[10:11], 6, v147
	v_cmp_eq_u32_e64 s[14:15], 7, v147
	v_pk_add_f32 v[38:39], v[60:61], v[90:91]
	v_pk_add_f32 v[50:51], v[58:59], v[118:119]
	v_pk_add_f32 v[54:55], v[82:83], v[152:153]
	v_pk_add_f32 v[58:59], v[122:123], v[154:155]
	v_pk_fma_f32 v[60:61], v[96:97], v[38:39], v[58:59] op_sel_hi:[0,1,1]
	v_pk_fma_f32 v[64:65], v[100:101], v[38:39], v[58:59] op_sel_hi:[0,1,1]
	v_pk_fma_f32 v[60:61], v[96:97], v[50:51], v[60:61] op_sel:[1,0,0]
	v_pk_fma_f32 v[64:65], v[100:101], v[50:51], v[64:65] op_sel:[1,0,0]
	v_pk_fma_f32 v[60:61], v[98:99], v[54:55], v[60:61] op_sel_hi:[0,1,1]
	v_pk_fma_f32 v[64:65], v[102:103], v[54:55], v[64:65] op_sel_hi:[0,1,1]
	v_pk_fma_f32 v[58:59], v[8:9], v[38:39], v[58:59] op_sel_hi:[0,1,1]
	v_pk_fma_f32 v[58:59], v[8:9], v[50:51], v[58:59] op_sel:[1,0,0]
	v_pk_fma_f32 v[58:59], v[10:11], v[54:55], v[58:59] op_sel_hi:[0,1,1]
	v_cndmask_b32_e64 v82, 0, v18, s[10:11]
	v_cndmask_b32_e64 v83, 0, v18, s[14:15]
	v_add_f32_dpp v58, v60, v58 wave_shl:1 row_mask:0xf bank_mask:0xf bound_ctrl:1
	v_add_f32_dpp v59, v61, v59 wave_shl:1 row_mask:0xf bank_mask:0xf bound_ctrl:1
	s_add_i32 s4, s34, 3
	s_cmpk_lt_i32 s4, 0x201
	s_cselect_b64 s[12:13], s[0:1], 0
	v_add_f32_dpp v58, v64, v58 wave_shr:1 row_mask:0xf bank_mask:0xf bound_ctrl:1
	v_add_f32_dpp v59, v65, v59 wave_shr:1 row_mask:0xf bank_mask:0xf bound_ctrl:1
	v_pk_fma_f32 v[58:59], v[4:5], v[146:147], v[58:59] op_sel_hi:[1,0,1] neg_lo:[0,0,1] neg_hi:[0,0,1]
	v_pk_add_f32 v[58:59], v[58:59], v[82:83] neg_lo:[0,1] neg_hi:[0,1]
	v_pk_mul_f32 v[122:123], v[58:59], v[58:59]
	v_add_f32_e32 v122, v122, v123
	v_cndmask_b32_e64 v123, 0, v122, s[12:13]
	v_add_f32_e32 v1, v1, v123
	s_add_i32 s5, s34, 8
	s_min_i32 s5, s5, 0x200
	s_mul_i32 s6, s5, 0x804
	s_add_i32 s6, s6, s35
	s_add_i32 s7, s6, 0x505014
	s_add_i32 s8, s6, 0x606018
	s_mul_i32 s9, s5, 0x180c
	s_add_i32 s9, s9, s33
	s_add_i32 s4, s34, 9
	s_min_i32 s4, s4, 0x200
	s_mul_i32 s4, s4, 0x804
	s_add_i32 s4, s4, s38
	buffer_load_dword v17, v28, s[20:23], s4 offen nt
	buffer_load_dwordx3 v[8:10], v27, s[24:27], s9 offen nt
	buffer_load_dword v4, v28, s[16:19], s7 offen nt
	buffer_load_dword v5, v28, s[16:19], s8 offen nt
	s_waitcnt vmcnt(8)
	v_mov_b32_dpp v96, v40 wave_shr:1 row_mask:0xf bank_mask:0xf bound_ctrl:1
	v_mov_b32_dpp v97, v41 wave_shr:1 row_mask:0xf bank_mask:0xf bound_ctrl:1
	v_mov_b32_dpp v98, v42 wave_shr:1 row_mask:0xf bank_mask:0xf bound_ctrl:1
	v_mov_b32_dpp v100, v40 wave_shl:1 row_mask:0xf bank_mask:0xf bound_ctrl:1
	v_mov_b32_dpp v101, v41 wave_shl:1 row_mask:0xf bank_mask:0xf bound_ctrl:1
	v_mov_b32_dpp v102, v42 wave_shl:1 row_mask:0xf bank_mask:0xf bound_ctrl:1
	s_add_i32 s4, s34, 7
	s_cmpk_lt_u32 s4, 0x201
	s_cselect_b64 s[12:13], s[40:41], 0
	v_cmp_eq_u32_e64 s[14:15], s37, v25
	s_and_b64 s[14:15], s[14:15], s[12:13]
	v_cndmask_b32_e64 v29, 0, 1, s[14:15]
	v_mul_f32_e64 v38, v40, v40
	v_mul_f32_e64 v39, v40, v41
	v_mul_f32_e64 v50, v40, v42
	v_mul_f32_e64 v51, v41, v41
	v_mul_f32_e64 v54, v41, v42
	v_mul_f32_e64 v55, v42, v42
	v_or_b32_dpp v31, v29, v29 wave_shr:1 row_mask:0xf bank_mask:0xf bound_ctrl:1
	s_nop 1
	v_or_b32_dpp v31, v29, v31 wave_shl:1 row_mask:0xf bank_mask:0xf bound_ctrl:1
	s_nop 1
	v_or_b32_dpp v53, v31, v31 wave_shr:1 row_mask:0xf bank_mask:0xf bound_ctrl:1
	s_nop 1
	v_or_b32_dpp v53, v31, v53 wave_shl:1 row_mask:0xf bank_mask:0xf bound_ctrl:1
	v_or3_b32 v29, v53, v84, v85
	v_or3_b32 v29, v29, v52, v30
	s_add_i32 s4, s34, 4
	s_cmpk_lt_u32 s4, 0x1ff
	s_cselect_b64 s[12:13], s[42:43], 0
	v_cmp_ne_u32_e64 s[30:31], 0, v29
	s_and_b64 s[30:31], s[30:31], s[12:13]
	v_cndmask_b32_e64 v29, 0, 1.0, s[30:31]
	v_add_f32_e64 v58, v40, v96
	v_add_f32_e64 v59, v41, v97
	v_add_f32_e64 v60, v42, v98
	v_fma_f32 v38, v96, v96, v38
	v_fma_f32 v39, v96, v97, v39
	v_fma_f32 v50, v96, v98, v50
	v_fma_f32 v51, v97, v97, v51
	v_fma_f32 v54, v97, v98, v54
	v_fma_f32 v55, v98, v98, v55
	v_add_f32_dpp v113, v29, v29 wave_shr:1 row_mask:0xf bank_mask:0xf bound_ctrl:1
	v_add_f32_e64 v58, v58, v100
	v_add_f32_e64 v59, v59, v101
	v_add_f32_e64 v60, v60, v102
	v_fma_f32 v61, v100, v100, v38
	v_fma_f32 v64, v100, v101, v39
	v_fma_f32 v65, v100, v102, v50
	v_fma_f32 v82, v101, v101, v51
	v_fma_f32 v83, v101, v102, v54
	v_fma_f32 v112, v102, v102, v55
	v_add_f32_dpp v113, v29, v113 wave_shl:1 row_mask:0xf bank_mask:0xf bound_ctrl:1
	v_pk_add_f32 v[38:39], v[124:125], v[58:59]
	v_pk_add_f32 v[50:51], v[56:57], v[38:39]
	v_pk_add_f32 v[54:55], v[126:127], v[60:61]
	v_pk_add_f32 v[56:57], v[62:63], v[54:55]
	v_pk_add_f32 v[62:63], v[130:131], v[64:65]
	v_pk_add_f32 v[114:115], v[66:67], v[62:63]
	v_pk_add_f32 v[66:67], v[136:137], v[82:83]
	v_pk_add_f32 v[122:123], v[86:87], v[66:67]
	v_pk_add_f32 v[86:87], v[138:139], v[112:113]
	v_pk_add_f32 v[124:125], v[88:89], v[86:87]
	v_mul_f32_e64 v136, v50, v22
	v_mul_f32_e64 v137, v51, v22
	v_mul_f32_e64 v138, v56, v22
	v_fma_f32 v29, v57, v22, v26
	v_mul_f32_e64 v31, v114, v22
	v_mul_f32_e64 v88, v115, v22
	v_fma_f32 v89, v122, v22, v26
	v_mul_f32_e64 v126, v123, v22
	v_fma_f32 v127, v124, v22, v26
	v_fma_f32 v29, -v136, v136, v29
	v_fma_f32 v31, -v136, v137, v31
	v_fma_f32 v88, -v136, v138, v88
	v_fma_f32 v89, -v137, v137, v89
	v_fma_f32 v126, -v137, v138, v126
	v_fma_f32 v127, -v138, v138, v127
	v_mul_f32_e64 v130, v126, v126
	v_mul_f32_e64 v131, v31, v127
	v_mul_f32_e64 v156, v88, v89
	v_mul_f32_e64 v157, v88, v88
	v_mul_f32_e64 v158, v29, v126
	v_mul_f32_e64 v159, v31, v31
	v_fma_f32 v130, v89, v127, -v130
	v_fma_f32 v131, v88, v126, -v131
	v_fma_f32 v156, v31, v126, -v156
	v_fma_f32 v157, v29, v127, -v157
	v_fma_f32 v158, v31, v88, -v158
	v_fma_f32 v159, v29, v89, -v159
	v_mul_f32_e64 v160, v29, v130
	v_fma_f32 v160, v31, v131, v160
	v_fma_f32 v160, v88, v156, v160
	v_rcp_f32_e32 v160, v160
	v_cmp_ne_u32_e64 vcc, s37, v2
	v_mul_f32_e64 v160, v160, v22
	v_cndmask_b32_e64 v160, 0, v160, s[30:31]
	v_cndmask_b32_e64 v29, 0, v18, vcc
	v_cndmask_b32_e64 v145, 0, v22, s[30:31]
	v_mul_f32_e64 v139, v130, v160
	v_mul_f32_e64 v140, v131, v160
	v_mul_f32_e64 v141, v156, v160
	v_mul_f32_e64 v142, v157, v160
	v_mul_f32_e64 v143, v158, v160
	v_mul_f32_e64 v144, v159, v160
	v_add_f32_e64 v146, v125, v29
	v_mov_b32_e32 v147, v2
	ds_write_b128 v23, v[136:139]
	ds_write_b128 v23, v[140:143] offset:1024
	ds_write_b128 v23, v[144:147] offset:2048
	s_waitcnt lgkmcnt(0)
	s_barrier
	v_mov_b32_dpp v30, v36 wave_shr:1 row_mask:0xf bank_mask:0xf bound_ctrl:1
	v_mov_b32_dpp v31, v37 wave_shr:1 row_mask:0xf bank_mask:0xf bound_ctrl:1
	v_mov_b32_dpp v50, v36 wave_shl:1 row_mask:0xf bank_mask:0xf bound_ctrl:1
	v_mov_b32_dpp v51, v37 wave_shl:1 row_mask:0xf bank_mask:0xf bound_ctrl:1
	v_pk_mul_f32 v[56:57], v[36:37], v[40:41] op_sel_hi:[1,0]
	v_pk_mul_f32 v[88:89], v[36:37], v[40:41] op_sel:[0,1]
	v_pk_mul_f32 v[114:115], v[36:37], v[42:43] op_sel_hi:[1,0]
	v_pk_add_f32 v[122:123], v[36:37], v[30:31]
	v_pk_fma_f32 v[56:57], v[30:31], v[96:97], v[56:57] op_sel_hi:[1,0,1]
	v_pk_fma_f32 v[88:89], v[30:31], v[96:97], v[88:89] op_sel:[0,1,0]
	v_pk_fma_f32 v[114:115], v[30:31], v[98:99], v[114:115] op_sel_hi:[1,0,1]
	v_pk_add_f32 v[122:123], v[122:123], v[50:51]
	v_pk_fma_f32 v[56:57], v[50:51], v[100:101], v[56:57] op_sel_hi:[1,0,1]
	v_pk_fma_f32 v[88:89], v[50:51], v[100:101], v[88:89] op_sel:[0,1,0]
	v_pk_fma_f32 v[114:115], v[50:51], v[102:103], v[114:115] op_sel_hi:[1,0,1]
	v_pk_add_f32 v[30:31], v[120:121], v[122:123]
	v_pk_add_f32 v[50:51], v[134:135], v[30:31]
	v_pk_add_f32 v[120:121], v[80:81], v[56:57]
	v_pk_add_f32 v[124:125], v[110:111], v[120:121]
	v_pk_add_f32 v[80:81], v[92:93], v[88:89]
	v_pk_add_f32 v[110:111], v[116:117], v[80:81]
	v_pk_add_f32 v[92:93], v[108:109], v[114:115]
	v_pk_add_f32 v[116:117], v[132:133], v[92:93]
	v_pk_fma_f32 v[124:125], v[136:137], v[50:51], v[124:125] op_sel_hi:[0,1,1] neg_lo:[1,0,0] neg_hi:[1,0,0]
	v_pk_fma_f32 v[110:111], v[136:137], v[50:51], v[110:111] op_sel:[1,0,0] neg_lo:[1,0,0] neg_hi:[1,0,0]
	v_pk_fma_f32 v[116:117], v[138:139], v[50:51], v[116:117] op_sel_hi:[0,1,1] neg_lo:[1,0,0] neg_hi:[1,0,0]
	v_pk_mul_f32 v[108:109], v[138:139], v[124:125] op_sel:[1,0]
	v_pk_mul_f32 v[126:127], v[140:141], v[124:125] op_sel_hi:[0,1]
	v_pk_mul_f32 v[130:131], v[140:141], v[124:125] op_sel:[1,0]
	v_pk_fma_f32 v[108:109], v[140:141], v[110:111], v[108:109] op_sel_hi:[0,1,1]
	v_pk_fma_f32 v[126:127], v[142:143], v[110:111], v[126:127] op_sel_hi:[0,1,1]
	v_pk_fma_f32 v[130:131], v[142:143], v[110:111], v[130:131] op_sel:[1,0,0]
	v_pk_fma_f32 v[108:109], v[140:141], v[116:117], v[108:109] op_sel:[1,0,0]
	v_pk_fma_f32 v[126:127], v[142:143], v[116:117], v[126:127] op_sel:[1,0,0]
	v_pk_fma_f32 v[130:131], v[144:145], v[116:117], v[130:131] op_sel_hi:[0,1,1]
	v_pk_mul_f32 v[132:133], v[136:137], v[108:109] op_sel_hi:[0,1]
	v_pk_fma_f32 v[132:133], v[136:137], v[126:127], v[132:133] op_sel:[1,0,0]
	v_pk_fma_f32 v[132:133], v[138:139], v[130:131], v[132:133] op_sel_hi:[0,1,1]
	v_pk_fma_f32 v[132:133], v[144:145], v[50:51], v[132:133] op_sel:[1,0,0] neg_lo:[0,0,1] neg_hi:[0,0,1]
	v_cmp_eq_u32_e64 s[10:11], 6, v147
	v_cmp_eq_u32_e64 s[14:15], 7, v147
	v_pk_add_f32 v[50:51], v[90:91], v[108:109]
	v_pk_add_f32 v[110:111], v[94:95], v[50:51]
	v_pk_add_f32 v[90:91], v[118:119], v[126:127]
	v_pk_add_f32 v[94:95], v[128:129], v[90:91]
	v_pk_add_f32 v[116:117], v[152:153], v[130:131]
	v_pk_add_f32 v[118:119], v[148:149], v[116:117]
	v_pk_add_f32 v[124:125], v[154:155], v[132:133]
	v_pk_add_f32 v[128:129], v[150:151], v[124:125]
	v_pk_fma_f32 v[134:135], v[44:45], v[110:111], v[128:129] op_sel_hi:[0,1,1]
	v_pk_fma_f32 v[148:149], v[68:69], v[110:111], v[128:129] op_sel_hi:[0,1,1]
	v_pk_fma_f32 v[134:135], v[44:45], v[94:95], v[134:135] op_sel:[1,0,0]
	v_pk_fma_f32 v[148:149], v[68:69], v[94:95], v[148:149] op_sel:[1,0,0]
	v_pk_fma_f32 v[134:135], v[46:47], v[118:119], v[134:135] op_sel_hi:[0,1,1]
	v_pk_fma_f32 v[148:149], v[70:71], v[118:119], v[148:149] op_sel_hi:[0,1,1]
	v_pk_fma_f32 v[128:129], v[12:13], v[110:111], v[128:129] op_sel_hi:[0,1,1]
	v_pk_fma_f32 v[128:129], v[12:13], v[94:95], v[128:129] op_sel:[1,0,0]
	v_pk_fma_f32 v[128:129], v[14:15], v[118:119], v[128:129] op_sel_hi:[0,1,1]
	v_cndmask_b32_e64 v150, 0, v18, s[10:11]
	v_cndmask_b32_e64 v151, 0, v18, s[14:15]
	v_add_f32_dpp v128, v134, v128 wave_shl:1 row_mask:0xf bank_mask:0xf bound_ctrl:1
	v_add_f32_dpp v129, v135, v129 wave_shl:1 row_mask:0xf bank_mask:0xf bound_ctrl:1
	s_add_i32 s4, s34, 4
	s_cmpk_lt_i32 s4, 0x201
	s_cselect_b64 s[12:13], s[0:1], 0
	v_add_f32_dpp v128, v148, v128 wave_shr:1 row_mask:0xf bank_mask:0xf bound_ctrl:1
	v_add_f32_dpp v129, v149, v129 wave_shr:1 row_mask:0xf bank_mask:0xf bound_ctrl:1
	v_pk_fma_f32 v[128:129], v[6:7], v[146:147], v[128:129] op_sel_hi:[1,0,1] neg_lo:[0,0,1] neg_hi:[0,0,1]
	v_pk_add_f32 v[128:129], v[128:129], v[150:151] neg_lo:[0,1] neg_hi:[0,1]
	v_pk_mul_f32 v[152:153], v[128:129], v[128:129]
	v_add_f32_e32 v152, v152, v153
	v_cndmask_b32_e64 v153, 0, v152, s[12:13]
	v_add_f32_e32 v1, v1, v153
	s_add_i32 s5, s34, 9
	s_min_i32 s5, s5, 0x200
	s_mul_i32 s6, s5, 0x804
	s_add_i32 s6, s6, s35
	s_add_i32 s7, s6, 0x505014
	s_add_i32 s8, s6, 0x606018
	s_mul_i32 s9, s5, 0x180c
	s_add_i32 s9, s9, s33
	s_add_i32 s4, s34, 10
	s_min_i32 s4, s4, 0x200
	s_mul_i32 s4, s4, 0x804
	s_add_i32 s4, s4, s38
	buffer_load_dword v2, v28, s[20:23], s4 offen nt
	buffer_load_dwordx3 v[12:14], v27, s[24:27], s9 offen nt
	buffer_load_dword v6, v28, s[16:19], s7 offen nt
	buffer_load_dword v7, v28, s[16:19], s8 offen nt
	s_waitcnt vmcnt(8)
	v_mov_b32_dpp v44, v72 wave_shr:1 row_mask:0xf bank_mask:0xf bound_ctrl:1
	v_mov_b32_dpp v45, v73 wave_shr:1 row_mask:0xf bank_mask:0xf bound_ctrl:1
	v_mov_b32_dpp v46, v74 wave_shr:1 row_mask:0xf bank_mask:0xf bound_ctrl:1
	v_mov_b32_dpp v68, v72 wave_shl:1 row_mask:0xf bank_mask:0xf bound_ctrl:1
	v_mov_b32_dpp v69, v73 wave_shl:1 row_mask:0xf bank_mask:0xf bound_ctrl:1
	v_mov_b32_dpp v70, v74 wave_shl:1 row_mask:0xf bank_mask:0xf bound_ctrl:1
	s_add_i32 s4, s34, 8
	s_cmpk_lt_u32 s4, 0x201
	s_cselect_b64 s[12:13], s[40:41], 0
	v_cmp_eq_u32_e64 s[14:15], s37, v24
	s_and_b64 s[14:15], s[14:15], s[12:13]
	v_cndmask_b32_e64 v29, 0, 1, s[14:15]
	v_mul_f32_e64 v94, v72, v72
	v_mul_f32_e64 v95, v72, v73
	v_mul_f32_e64 v110, v72, v74
	v_mul_f32_e64 v111, v73, v73
	v_mul_f32_e64 v118, v73, v74
	v_mul_f32_e64 v119, v74, v74
	v_or_b32_dpp v128, v29, v29 wave_shr:1 row_mask:0xf bank_mask:0xf bound_ctrl:1
	s_nop 1
	v_or_b32_dpp v128, v29, v128 wave_shl:1 row_mask:0xf bank_mask:0xf bound_ctrl:1
	s_nop 1
	v_or_b32_dpp v129, v128, v128 wave_shr:1 row_mask:0xf bank_mask:0xf bound_ctrl:1
	s_nop 1
	v_or_b32_dpp v129, v128, v129 wave_shl:1 row_mask:0xf bank_mask:0xf bound_ctrl:1
	v_or3_b32 v29, v129, v53, v84
	v_or3_b32 v29, v29, v85, v52
	s_add_i32 s4, s34, 5
	s_cmpk_lt_u32 s4, 0x1ff
	s_cselect_b64 s[12:13], s[42:43], 0
	v_cmp_ne_u32_e64 s[30:31], 0, v29
	s_and_b64 s[30:31], s[30:31], s[12:13]
	v_cndmask_b32_e64 v29, 0, 1.0, s[30:31]
	v_add_f32_e64 v134, v72, v44
	v_add_f32_e64 v135, v73, v45
	v_add_f32_e64 v136, v74, v46
	v_fma_f32 v94, v44, v44, v94
	v_fma_f32 v95, v44, v45, v95
	v_fma_f32 v110, v44, v46, v110
	v_fma_f32 v111, v45, v45, v111
	v_fma_f32 v118, v45, v46, v118
	v_fma_f32 v119, v46, v46, v119
	v_add_f32_dpp v143, v29, v29 wave_shr:1 row_mask:0xf bank_mask:0xf bound_ctrl:1
	v_add_f32_e64 v134, v134, v68
	v_add_f32_e64 v135, v135, v69
	v_add_f32_e64 v136, v136, v70
	v_fma_f32 v137, v68, v68, v94
	v_fma_f32 v138, v68, v69, v95
	v_fma_f32 v139, v68, v70, v110
	v_fma_f32 v140, v69, v69, v111
	v_fma_f32 v141, v69, v70, v118
	v_fma_f32 v142, v70, v70, v119
	v_add_f32_dpp v143, v29, v143 wave_shl:1 row_mask:0xf bank_mask:0xf bound_ctrl:1
	v_pk_add_f32 v[94:95], v[38:39], v[134:135]
	v_pk_add_f32 v[38:39], v[54:55], v[136:137]
	v_pk_add_f32 v[54:55], v[62:63], v[138:139]
	v_pk_add_f32 v[62:63], v[66:67], v[140:141]
	v_pk_add_f32 v[66:67], v[86:87], v[142:143]
	v_mul_f32_e64 v144, v94, v22
	v_mul_f32_e64 v145, v95, v22
	v_mul_f32_e64 v146, v38, v22
	v_fma_f32 v29, v39, v22, v26
	v_mul_f32_e64 v128, v54, v22
	v_mul_f32_e64 v86, v55, v22
	v_fma_f32 v87, v62, v22, v26
	v_mul_f32_e64 v110, v63, v22
	v_fma_f32 v111, v66, v22, v26
	v_fma_f32 v29, -v144, v144, v29
	v_fma_f32 v128, -v144, v145, v128
	v_fma_f32 v86, -v144, v146, v86
	v_fma_f32 v87, -v145, v145, v87
	v_fma_f32 v110, -v145, v146, v110
	v_fma_f32 v111, -v146, v146, v111
	v_mul_f32_e64 v118, v110, v110
	v_mul_f32_e64 v119, v128, v111
	v_mul_f32_e64 v156, v86, v87
	v_mul_f32_e64 v157, v86, v86
	v_mul_f32_e64 v158, v29, v110
	v_mul_f32_e64 v159, v128, v128
	v_fma_f32 v118, v87, v111, -v118
	v_fma_f32 v119, v86, v110, -v119
	v_fma_f32 v156, v128, v110, -v156
	v_fma_f32 v157, v29, v111, -v157
	v_fma_f32 v158, v128, v86, -v158
	v_fma_f32 v159, v29, v87, -v159
	v_mul_f32_e64 v160, v29, v118
	v_fma_f32 v160, v128, v119, v160
	v_fma_f32 v160, v86, v156, v160
	v_rcp_f32_e32 v160, v160
	v_cmp_ne_u32_e64 vcc, s37, v3
	v_mul_f32_e64 v160, v160, v22
	v_cndmask_b32_e64 v160, 0, v160, s[30:31]
	v_cndmask_b32_e64 v29, 0, v18, vcc
	v_cndmask_b32_e64 v153, 0, v22, s[30:31]
	v_mul_f32_e64 v147, v118, v160
	v_mul_f32_e64 v148, v119, v160
	v_mul_f32_e64 v149, v156, v160
	v_mul_f32_e64 v150, v157, v160
	v_mul_f32_e64 v151, v158, v160
	v_mul_f32_e64 v152, v159, v160
	v_add_f32_e64 v154, v67, v29
	v_mov_b32_e32 v155, v3
	ds_write_b128 v23, v[144:147] offset:3072
	ds_write_b128 v23, v[148:151] offset:4096
	ds_write_b128 v23, v[152:155] offset:5120
	s_waitcnt lgkmcnt(0)
	s_barrier
	v_mov_b32_dpp v38, v48 wave_shr:1 row_mask:0xf bank_mask:0xf bound_ctrl:1
	v_mov_b32_dpp v39, v49 wave_shr:1 row_mask:0xf bank_mask:0xf bound_ctrl:1
	v_mov_b32_dpp v54, v48 wave_shl:1 row_mask:0xf bank_mask:0xf bound_ctrl:1
	v_mov_b32_dpp v55, v49 wave_shl:1 row_mask:0xf bank_mask:0xf bound_ctrl:1
	v_pk_mul_f32 v[62:63], v[48:49], v[72:73] op_sel_hi:[1,0]
	v_pk_mul_f32 v[66:67], v[48:49], v[72:73] op_sel:[0,1]
	v_pk_mul_f32 v[86:87], v[48:49], v[74:75] op_sel_hi:[1,0]
	v_pk_add_f32 v[94:95], v[48:49], v[38:39]
	v_pk_fma_f32 v[62:63], v[38:39], v[44:45], v[62:63] op_sel_hi:[1,0,1]
	v_pk_fma_f32 v[66:67], v[38:39], v[44:45], v[66:67] op_sel:[0,1,0]
	v_pk_fma_f32 v[86:87], v[38:39], v[46:47], v[86:87] op_sel_hi:[1,0,1]
	v_pk_add_f32 v[94:95], v[94:95], v[54:55]
	v_pk_fma_f32 v[62:63], v[54:55], v[68:69], v[62:63] op_sel_hi:[1,0,1]
	v_pk_fma_f32 v[66:67], v[54:55], v[68:69], v[66:67] op_sel:[0,1,0]
	v_pk_fma_f32 v[86:87], v[54:55], v[70:71], v[86:87] op_sel_hi:[1,0,1]
	v_pk_add_f32 v[38:39], v[30:31], v[94:95]
	v_pk_add_f32 v[30:31], v[120:121], v[62:63]
	v_pk_add_f32 v[54:55], v[80:81], v[66:67]
	v_pk_add_f32 v[80:81], v[92:93], v[86:87]
	v_pk_fma_f32 v[30:31], v[144:145], v[38:39], v[30:31] op_sel_hi:[0,1,1] neg_lo:[1,0,0] neg_hi:[1,0,0]
	v_pk_fma_f32 v[54:55], v[144:145], v[38:39], v[54:55] op_sel:[1,0,0] neg_lo:[1,0,0] neg_hi:[1,0,0]
	v_pk_fma_f32 v[80:81], v[146:147], v[38:39], v[80:81] op_sel_hi:[0,1,1] neg_lo:[1,0,0] neg_hi:[1,0,0]
	v_pk_mul_f32 v[92:93], v[146:147], v[30:31] op_sel:[1,0]
	v_pk_mul_f32 v[110:111], v[148:149], v[30:31] op_sel_hi:[0,1]
	v_pk_mul_f32 v[118:119], v[148:149], v[30:31] op_sel:[1,0]
	v_pk_fma_f32 v[92:93], v[148:149], v[54:55], v[92:93] op_sel_hi:[0,1,1]
	v_pk_fma_f32 v[110:111], v[150:151], v[54:55], v[110:111] op_sel_hi:[0,1,1]
	v_pk_fma_f32 v[118:119], v[150:151], v[54:55], v[118:119] op_sel:[1,0,0]
	v_pk_fma_f32 v[92:93], v[148:149], v[80:81], v[92:93] op_sel:[1,0,0]
	v_pk_fma_f32 v[110:111], v[150:151], v[80:81], v[110:111] op_sel:[1,0,0]
	v_pk_fma_f32 v[118:119], v[152:153], v[80:81], v[118:119] op_sel_hi:[0,1,1]
	v_pk_mul_f32 v[120:121], v[144:145], v[92:93] op_sel_hi:[0,1]
	v_pk_fma_f32 v[120:121], v[144:145], v[110:111], v[120:121] op_sel:[1,0,0]
	v_pk_fma_f32 v[120:121], v[146:147], v[118:119], v[120:121] op_sel_hi:[0,1,1]
	v_pk_fma_f32 v[120:121], v[152:153], v[38:39], v[120:121] op_sel:[1,0,0] neg_lo:[0,0,1] neg_hi:[0,0,1]
	v_cmp_eq_u32_e64 s[10:11], 6, v155
	v_cmp_eq_u32_e64 s[14:15], 7, v155
	v_pk_add_f32 v[30:31], v[50:51], v[92:93]
	v_pk_add_f32 v[38:39], v[90:91], v[110:111]
	v_pk_add_f32 v[50:51], v[116:117], v[118:119]
	v_pk_add_f32 v[54:55], v[124:125], v[120:121]
	v_pk_fma_f32 v[80:81], v[76:77], v[30:31], v[54:55] op_sel_hi:[0,1,1]
	v_pk_fma_f32 v[90:91], v[104:105], v[30:31], v[54:55] op_sel_hi:[0,1,1]
	v_pk_fma_f32 v[80:81], v[76:77], v[38:39], v[80:81] op_sel:[1,0,0]
	v_pk_fma_f32 v[90:91], v[104:105], v[38:39], v[90:91] op_sel:[1,0,0]
	v_pk_fma_f32 v[80:81], v[78:79], v[50:51], v[80:81] op_sel_hi:[0,1,1]
	v_pk_fma_f32 v[90:91], v[106:107], v[50:51], v[90:91] op_sel_hi:[0,1,1]
	v_pk_fma_f32 v[54:55], v[32:33], v[30:31], v[54:55] op_sel_hi:[0,1,1]
	v_pk_fma_f32 v[54:55], v[32:33], v[38:39], v[54:55] op_sel:[1,0,0]
	v_pk_fma_f32 v[54:55], v[34:35], v[50:51], v[54:55] op_sel_hi:[0,1,1]
	v_cndmask_b32_e64 v116, 0, v18, s[10:11]
	v_cndmask_b32_e64 v117, 0, v18, s[14:15]
	v_add_f32_dpp v54, v80, v54 wave_shl:1 row_mask:0xf bank_mask:0xf bound_ctrl:1
	v_add_f32_dpp v55, v81, v55 wave_shl:1 row_mask:0xf bank_mask:0xf bound_ctrl:1
	s_add_i32 s4, s34, 5
	s_cmpk_lt_i32 s4, 0x201
	s_cselect_b64 s[12:13], s[0:1], 0
	v_add_f32_dpp v54, v90, v54 wave_shr:1 row_mask:0xf bank_mask:0xf bound_ctrl:1
	v_add_f32_dpp v55, v91, v55 wave_shr:1 row_mask:0xf bank_mask:0xf bound_ctrl:1
	v_pk_fma_f32 v[54:55], v[20:21], v[154:155], v[54:55] op_sel_hi:[1,0,1] neg_lo:[0,0,1] neg_hi:[0,0,1]
	v_pk_add_f32 v[54:55], v[54:55], v[116:117] neg_lo:[0,1] neg_hi:[0,1]
	v_pk_mul_f32 v[124:125], v[54:55], v[54:55]
	v_add_f32_e32 v124, v124, v125
	v_cndmask_b32_e64 v125, 0, v124, s[12:13]
	v_add_f32_e32 v1, v1, v125
	s_add_i32 s5, s34, 10
	s_min_i32 s5, s5, 0x200
	s_mul_i32 s6, s5, 0x804
	s_add_i32 s6, s6, s35
	s_add_i32 s7, s6, 0x505014
	s_add_i32 s8, s6, 0x606018
	s_mul_i32 s9, s5, 0x180c
	s_add_i32 s9, s9, s33
	s_add_i32 s4, s34, 11
	s_min_i32 s4, s4, 0x200
	s_mul_i32 s4, s4, 0x804
	s_add_i32 s4, s4, s38
	buffer_load_dword v3, v28, s[20:23], s4 offen nt
	buffer_load_dwordx3 v[32:34], v27, s[24:27], s9 offen nt
	buffer_load_dword v20, v28, s[16:19], s7 offen nt
	buffer_load_dword v21, v28, s[16:19], s8 offen nt
	s_waitcnt vmcnt(8)
	v_mov_b32_dpp v76, v8 wave_shr:1 row_mask:0xf bank_mask:0xf bound_ctrl:1
	v_mov_b32_dpp v77, v9 wave_shr:1 row_mask:0xf bank_mask:0xf bound_ctrl:1
	v_mov_b32_dpp v78, v10 wave_shr:1 row_mask:0xf bank_mask:0xf bound_ctrl:1
	v_mov_b32_dpp v104, v8 wave_shl:1 row_mask:0xf bank_mask:0xf bound_ctrl:1
	v_mov_b32_dpp v105, v9 wave_shl:1 row_mask:0xf bank_mask:0xf bound_ctrl:1
	v_mov_b32_dpp v106, v10 wave_shl:1 row_mask:0xf bank_mask:0xf bound_ctrl:1
	s_add_i32 s4, s34, 9
	s_cmpk_lt_u32 s4, 0x201
	s_cselect_b64 s[12:13], s[40:41], 0
	v_cmp_eq_u32_e64 s[14:15], s37, v17
	s_and_b64 s[14:15], s[14:15], s[12:13]
	v_cndmask_b32_e64 v29, 0, 1, s[14:15]
	v_mul_f32_e64 v30, v8, v8
	v_mul_f32_e64 v31, v8, v9
	v_mul_f32_e64 v38, v8, v10
	v_mul_f32_e64 v39, v9, v9
	v_mul_f32_e64 v50, v9, v10
	v_mul_f32_e64 v51, v10, v10
	v_or_b32_dpp v52, v29, v29 wave_shr:1 row_mask:0xf bank_mask:0xf bound_ctrl:1
	s_nop 1
	v_or_b32_dpp v52, v29, v52 wave_shl:1 row_mask:0xf bank_mask:0xf bound_ctrl:1
	s_nop 1
	v_or_b32_dpp v128, v52, v52 wave_shr:1 row_mask:0xf bank_mask:0xf bound_ctrl:1
	s_nop 1
	v_or_b32_dpp v128, v52, v128 wave_shl:1 row_mask:0xf bank_mask:0xf bound_ctrl:1
	v_or3_b32 v29, v128, v129, v53
	v_or3_b32 v29, v29, v84, v85
	s_add_i32 s4, s34, 6
	s_cmpk_lt_u32 s4, 0x1ff
	s_cselect_b64 s[12:13], s[42:43], 0
	v_cmp_ne_u32_e64 s[30:31], 0, v29
	s_and_b64 s[30:31], s[30:31], s[12:13]
	v_cndmask_b32_e64 v29, 0, 1.0, s[30:31]
	v_add_f32_e64 v54, v8, v76
	v_add_f32_e64 v55, v9, v77
	v_add_f32_e64 v80, v10, v78
	v_fma_f32 v30, v76, v76, v30
	v_fma_f32 v31, v76, v77, v31
	v_fma_f32 v38, v76, v78, v38
	v_fma_f32 v39, v77, v77, v39
	v_fma_f32 v50, v77, v78, v50
	v_fma_f32 v51, v78, v78, v51
	v_add_f32_dpp v125, v29, v29 wave_shr:1 row_mask:0xf bank_mask:0xf bound_ctrl:1
	v_add_f32_e64 v54, v54, v104
	v_add_f32_e64 v55, v55, v105
	v_add_f32_e64 v80, v80, v106
	v_fma_f32 v81, v104, v104, v30
	v_fma_f32 v90, v104, v105, v31
	v_fma_f32 v91, v104, v106, v38
	v_fma_f32 v116, v105, v105, v39
	v_fma_f32 v117, v105, v106, v50
	v_fma_f32 v124, v106, v106, v51
	v_add_f32_dpp v125, v29, v125 wave_shl:1 row_mask:0xf bank_mask:0xf bound_ctrl:1
	v_pk_add_f32 v[30:31], v[134:135], v[54:55]
	v_pk_add_f32 v[38:39], v[58:59], v[30:31]
	v_pk_add_f32 v[50:51], v[136:137], v[80:81]
	v_pk_add_f32 v[58:59], v[60:61], v[50:51]
	v_pk_add_f32 v[60:61], v[138:139], v[90:91]
	v_pk_add_f32 v[134:135], v[64:65], v[60:61]
	v_pk_add_f32 v[64:65], v[140:141], v[116:117]
	v_pk_add_f32 v[136:137], v[82:83], v[64:65]
	v_pk_add_f32 v[82:83], v[142:143], v[124:125]
	v_pk_add_f32 v[138:139], v[112:113], v[82:83]
	v_mul_f32_e64 v140, v38, v22
	v_mul_f32_e64 v141, v39, v22
	v_mul_f32_e64 v142, v58, v22
	v_fma_f32 v29, v59, v22, v26
	v_mul_f32_e64 v52, v134, v22
	v_mul_f32_e64 v112, v135, v22
	v_fma_f32 v113, v136, v22, v26
	v_mul_f32_e64 v152, v137, v22
	v_fma_f32 v153, v138, v22, v26
	v_fma_f32 v29, -v140, v140, v29
	v_fma_f32 v52, -v140, v141, v52
	v_fma_f32 v112, -v140, v142, v112
	v_fma_f32 v113, -v141, v141, v113
	v_fma_f32 v152, -v141, v142, v152
	v_fma_f32 v153, -v142, v142, v153
	v_mul_f32_e64 v154, v152, v152
	v_mul_f32_e64 v155, v52, v153
	v_mul_f32_e64 v156, v112, v113
	v_mul_f32_e64 v157, v112, v112
	v_mul_f32_e64 v158, v29, v152
	v_mul_f32_e64 v159, v52, v52
	v_fma_f32 v154, v113, v153, -v154
	v_fma_f32 v155, v112, v152, -v155
	v_fma_f32 v156, v52, v152, -v156
	v_fma_f32 v157, v29, v153, -v157
	v_fma_f32 v158, v52, v112, -v158
	v_fma_f32 v159, v29, v113, -v159
	v_mul_f32_e64 v160, v29, v154
	v_fma_f32 v160, v52, v155, v160
	v_fma_f32 v160, v112, v156, v160
	v_rcp_f32_e32 v160, v160
	v_cmp_ne_u32_e64 vcc, s37, v16
	v_mul_f32_e64 v160, v160, v22
	v_cndmask_b32_e64 v160, 0, v160, s[30:31]
	v_cndmask_b32_e64 v29, 0, v18, vcc
	v_cndmask_b32_e64 v149, 0, v22, s[30:31]
	v_mul_f32_e64 v143, v154, v160
	v_mul_f32_e64 v144, v155, v160
	v_mul_f32_e64 v145, v156, v160
	v_mul_f32_e64 v146, v157, v160
	v_mul_f32_e64 v147, v158, v160
	v_mul_f32_e64 v148, v159, v160
	v_add_f32_e64 v150, v139, v29
	v_mov_b32_e32 v151, v16
	ds_write_b128 v23, v[140:143]
	ds_write_b128 v23, v[144:147] offset:1024
	ds_write_b128 v23, v[148:151] offset:2048
	s_waitcnt lgkmcnt(0)
	s_barrier
	v_mov_b32_dpp v38, v4 wave_shr:1 row_mask:0xf bank_mask:0xf bound_ctrl:1
	v_mov_b32_dpp v39, v5 wave_shr:1 row_mask:0xf bank_mask:0xf bound_ctrl:1
	v_mov_b32_dpp v58, v4 wave_shl:1 row_mask:0xf bank_mask:0xf bound_ctrl:1
	v_mov_b32_dpp v59, v5 wave_shl:1 row_mask:0xf bank_mask:0xf bound_ctrl:1
	v_pk_mul_f32 v[112:113], v[4:5], v[8:9] op_sel_hi:[1,0]
	v_pk_mul_f32 v[134:135], v[4:5], v[8:9] op_sel:[0,1]
	v_pk_mul_f32 v[136:137], v[4:5], v[10:11] op_sel_hi:[1,0]
	v_pk_add_f32 v[138:139], v[4:5], v[38:39]
	v_pk_fma_f32 v[112:113], v[38:39], v[76:77], v[112:113] op_sel_hi:[1,0,1]
	v_pk_fma_f32 v[134:135], v[38:39], v[76:77], v[134:135] op_sel:[0,1,0]
	v_pk_fma_f32 v[136:137], v[38:39], v[78:79], v[136:137] op_sel_hi:[1,0,1]
	v_pk_add_f32 v[138:139], v[138:139], v[58:59]
	v_pk_fma_f32 v[112:113], v[58:59], v[104:105], v[112:113] op_sel_hi:[1,0,1]
	v_pk_fma_f32 v[134:135], v[58:59], v[104:105], v[134:135] op_sel:[0,1,0]
	v_pk_fma_f32 v[136:137], v[58:59], v[106:107], v[136:137] op_sel_hi:[1,0,1]
	v_pk_add_f32 v[38:39], v[94:95], v[138:139]
	v_pk_add_f32 v[58:59], v[122:123], v[38:39]
	v_pk_add_f32 v[94:95], v[62:63], v[112:113]
	v_pk_add_f32 v[122:123], v[56:57], v[94:95]
	v_pk_add_f32 v[56:57], v[66:67], v[134:135]
	v_pk_add_f32 v[62:63], v[88:89], v[56:57]
	v_pk_add_f32 v[66:67], v[86:87], v[136:137]
	v_pk_add_f32 v[88:89], v[114:115], v[66:67]
	v_pk_fma_f32 v[122:123], v[140:141], v[58:59], v[122:123] op_sel_hi:[0,1,1] neg_lo:[1,0,0] neg_hi:[1,0,0]
	v_pk_fma_f32 v[62:63], v[140:141], v[58:59], v[62:63] op_sel:[1,0,0] neg_lo:[1,0,0] neg_hi:[1,0,0]
	v_pk_fma_f32 v[88:89], v[142:143], v[58:59], v[88:89] op_sel_hi:[0,1,1] neg_lo:[1,0,0] neg_hi:[1,0,0]
	v_pk_mul_f32 v[86:87], v[142:143], v[122:123] op_sel:[1,0]
	v_pk_mul_f32 v[114:115], v[144:145], v[122:123] op_sel_hi:[0,1]
	v_pk_mul_f32 v[152:153], v[144:145], v[122:123] op_sel:[1,0]
	v_pk_fma_f32 v[86:87], v[144:145], v[62:63], v[86:87] op_sel_hi:[0,1,1]
	v_pk_fma_f32 v[114:115], v[146:147], v[62:63], v[114:115] op_sel_hi:[0,1,1]
	v_pk_fma_f32 v[152:153], v[146:147], v[62:63], v[152:153] op_sel:[1,0,0]
	v_pk_fma_f32 v[86:87], v[144:145], v[88:89], v[86:87] op_sel:[1,0,0]
	v_pk_fma_f32 v[114:115], v[146:147], v[88:89], v[114:115] op_sel:[1,0,0]
	v_pk_fma_f32 v[152:153], v[148:149], v[88:89], v[152:153] op_sel_hi:[0,1,1]
	v_pk_mul_f32 v[154:155], v[140:141], v[86:87] op_sel_hi:[0,1]
	v_pk_fma_f32 v[154:155], v[140:141], v[114:115], v[154:155] op_sel:[1,0,0]
	v_pk_fma_f32 v[154:155], v[142:143], v[152:153], v[154:155] op_sel_hi:[0,1,1]
	v_pk_fma_f32 v[154:155], v[148:149], v[58:59], v[154:155] op_sel:[1,0,0] neg_lo:[0,0,1] neg_hi:[0,0,1]
	v_cmp_eq_u32_e64 s[10:11], 6, v151
	v_cmp_eq_u32_e64 s[14:15], 7, v151
	v_pk_add_f32 v[58:59], v[92:93], v[86:87]
	v_pk_add_f32 v[62:63], v[108:109], v[58:59]
	v_pk_add_f32 v[88:89], v[110:111], v[114:115]
	v_pk_add_f32 v[92:93], v[126:127], v[88:89]
	v_pk_add_f32 v[108:109], v[118:119], v[152:153]
	v_pk_add_f32 v[110:111], v[130:131], v[108:109]
	v_pk_add_f32 v[118:119], v[120:121], v[154:155]
	v_pk_add_f32 v[122:123], v[132:133], v[118:119]
	v_pk_fma_f32 v[120:121], v[96:97], v[62:63], v[122:123] op_sel_hi:[0,1,1]
	v_pk_fma_f32 v[126:127], v[100:101], v[62:63], v[122:123] op_sel_hi:[0,1,1]
	v_pk_fma_f32 v[120:121], v[96:97], v[92:93], v[120:121] op_sel:[1,0,0]
	v_pk_fma_f32 v[126:127], v[100:101], v[92:93], v[126:127] op_sel:[1,0,0]
	v_pk_fma_f32 v[120:121], v[98:99], v[110:111], v[120:121] op_sel_hi:[0,1,1]
	v_pk_fma_f32 v[126:127], v[102:103], v[110:111], v[126:127] op_sel_hi:[0,1,1]
	v_pk_fma_f32 v[122:123], v[40:41], v[62:63], v[122:123] op_sel_hi:[0,1,1]
	v_pk_fma_f32 v[122:123], v[40:41], v[92:93], v[122:123] op_sel:[1,0,0]
	v_pk_fma_f32 v[122:123], v[42:43], v[110:111], v[122:123] op_sel_hi:[0,1,1]
	v_cndmask_b32_e64 v130, 0, v18, s[10:11]
	v_cndmask_b32_e64 v131, 0, v18, s[14:15]
	v_add_f32_dpp v122, v120, v122 wave_shl:1 row_mask:0xf bank_mask:0xf bound_ctrl:1
	v_add_f32_dpp v123, v121, v123 wave_shl:1 row_mask:0xf bank_mask:0xf bound_ctrl:1
	s_add_i32 s4, s34, 6
	s_cmpk_lt_i32 s4, 0x201
	s_cselect_b64 s[12:13], s[0:1], 0
	v_add_f32_dpp v122, v126, v122 wave_shr:1 row_mask:0xf bank_mask:0xf bound_ctrl:1
	v_add_f32_dpp v123, v127, v123 wave_shr:1 row_mask:0xf bank_mask:0xf bound_ctrl:1
	v_pk_fma_f32 v[122:123], v[36:37], v[150:151], v[122:123] op_sel_hi:[1,0,1] neg_lo:[0,0,1] neg_hi:[0,0,1]
	v_pk_add_f32 v[122:123], v[122:123], v[130:131] neg_lo:[0,1] neg_hi:[0,1]
	v_pk_mul_f32 v[132:133], v[122:123], v[122:123]
	v_add_f32_e32 v132, v132, v133
	v_cndmask_b32_e64 v133, 0, v132, s[12:13]
	v_add_f32_e32 v1, v1, v133
	s_add_i32 s5, s34, 11
	s_min_i32 s5, s5, 0x200
	s_mul_i32 s6, s5, 0x804
	s_add_i32 s6, s6, s35
	s_add_i32 s7, s6, 0x505014
	s_add_i32 s8, s6, 0x606018
	s_mul_i32 s9, s5, 0x180c
	s_add_i32 s9, s9, s33
	s_add_i32 s4, s34, 12
	s_min_i32 s4, s4, 0x200
	s_mul_i32 s4, s4, 0x804
	s_add_i32 s4, s4, s38
	buffer_load_dword v16, v28, s[20:23], s4 offen nt
	buffer_load_dwordx3 v[40:42], v27, s[24:27], s9 offen nt
	buffer_load_dword v36, v28, s[16:19], s7 offen nt
	buffer_load_dword v37, v28, s[16:19], s8 offen nt
	s_waitcnt vmcnt(8)
	v_mov_b32_dpp v96, v12 wave_shr:1 row_mask:0xf bank_mask:0xf bound_ctrl:1
	v_mov_b32_dpp v97, v13 wave_shr:1 row_mask:0xf bank_mask:0xf bound_ctrl:1
	v_mov_b32_dpp v98, v14 wave_shr:1 row_mask:0xf bank_mask:0xf bound_ctrl:1
	v_mov_b32_dpp v100, v12 wave_shl:1 row_mask:0xf bank_mask:0xf bound_ctrl:1
	v_mov_b32_dpp v101, v13 wave_shl:1 row_mask:0xf bank_mask:0xf bound_ctrl:1
	v_mov_b32_dpp v102, v14 wave_shl:1 row_mask:0xf bank_mask:0xf bound_ctrl:1
	s_add_i32 s4, s34, 10
	s_cmpk_lt_u32 s4, 0x201
	s_cselect_b64 s[12:13], s[40:41], 0
	v_cmp_eq_u32_e64 s[14:15], s37, v2
	s_and_b64 s[14:15], s[14:15], s[12:13]
	v_cndmask_b32_e64 v29, 0, 1, s[14:15]
	v_mul_f32_e64 v62, v12, v12
	v_mul_f32_e64 v63, v12, v13
	v_mul_f32_e64 v92, v12, v14
	v_mul_f32_e64 v93, v13, v13
	v_mul_f32_e64 v110, v13, v14
	v_mul_f32_e64 v111, v14, v14
	v_or_b32_dpp v52, v29, v29 wave_shr:1 row_mask:0xf bank_mask:0xf bound_ctrl:1
	s_nop 1
	v_or_b32_dpp v52, v29, v52 wave_shl:1 row_mask:0xf bank_mask:0xf bound_ctrl:1
	s_nop 1
	v_or_b32_dpp v85, v52, v52 wave_shr:1 row_mask:0xf bank_mask:0xf bound_ctrl:1
	s_nop 1
	v_or_b32_dpp v85, v52, v85 wave_shl:1 row_mask:0xf bank_mask:0xf bound_ctrl:1
	v_or3_b32 v29, v85, v128, v129
	v_or3_b32 v29, v29, v53, v84
	s_add_i32 s4, s34, 7
	s_cmpk_lt_u32 s4, 0x1ff
	s_cselect_b64 s[12:13], s[42:43], 0
	v_cmp_ne_u32_e64 s[30:31], 0, v29
	s_and_b64 s[30:31], s[30:31], s[12:13]
	v_cndmask_b32_e64 v29, 0, 1.0, s[30:31]
	v_add_f32_e64 v120, v12, v96
	v_add_f32_e64 v121, v13, v97
	v_add_f32_e64 v122, v14, v98
	v_fma_f32 v62, v96, v96, v62
	v_fma_f32 v63, v96, v97, v63
	v_fma_f32 v92, v96, v98, v92
	v_fma_f32 v93, v97, v97, v93
	v_fma_f32 v110, v97, v98, v110
	v_fma_f32 v111, v98, v98, v111
	v_add_f32_dpp v133, v29, v29 wave_shr:1 row_mask:0xf bank_mask:0xf bound_ctrl:1
	v_add_f32_e64 v120, v120, v100
	v_add_f32_e64 v121, v121, v101
	v_add_f32_e64 v122, v122, v102
	v_fma_f32 v123, v100, v100, v62
	v_fma_f32 v126, v100, v101, v63
	v_fma_f32 v127, v100, v102, v92
	v_fma_f32 v130, v101, v101, v93
	v_fma_f32 v131, v101, v102, v110
	v_fma_f32 v132, v102, v102, v111
	v_add_f32_dpp v133, v29, v133 wave_shl:1 row_mask:0xf bank_mask:0xf bound_ctrl:1
	v_pk_add_f32 v[62:63], v[30:31], v[120:121]
	v_pk_add_f32 v[30:31], v[50:51], v[122:123]
	v_pk_add_f32 v[50:51], v[60:61], v[126:127]
	v_pk_add_f32 v[60:61], v[64:65], v[130:131]
	v_pk_add_f32 v[64:65], v[82:83], v[132:133]
	v_mul_f32_e64 v140, v62, v22
	v_mul_f32_e64 v141, v63, v22
	v_mul_f32_e64 v142, v30, v22
	v_fma_f32 v29, v31, v22, v26
	v_mul_f32_e64 v52, v50, v22
	v_mul_f32_e64 v82, v51, v22
	v_fma_f32 v83, v60, v22, v26
	v_mul_f32_e64 v92, v61, v22
	v_fma_f32 v93, v64, v22, v26
	v_fma_f32 v29, -v140, v140, v29
	v_fma_f32 v52, -v140, v141, v52
	v_fma_f32 v82, -v140, v142, v82
	v_fma_f32 v83, -v141, v141, v83
	v_fma_f32 v92, -v141, v142, v92
	v_fma_f32 v93, -v142, v142, v93
	v_mul_f32_e64 v110, v92, v92
	v_mul_f32_e64 v111, v52, v93
	v_mul_f32_e64 v156, v82, v83
	v_mul_f32_e64 v157, v82, v82
	v_mul_f32_e64 v158, v29, v92
	v_mul_f32_e64 v159, v52, v52
	v_fma_f32 v110, v83, v93, -v110
	v_fma_f32 v111, v82, v92, -v111
	v_fma_f32 v156, v52, v92, -v156
	v_fma_f32 v157, v29, v93, -v157
	v_fma_f32 v158, v52, v82, -v158
	v_fma_f32 v159, v29, v83, -v159
	v_mul_f32_e64 v160, v29, v110
	v_fma_f32 v160, v52, v111, v160
	v_fma_f32 v160, v82, v156, v160
	v_rcp_f32_e32 v160, v160
	v_cmp_ne_u32_e64 vcc, s37, v25
	v_mul_f32_e64 v160, v160, v22
	v_cndmask_b32_e64 v160, 0, v160, s[30:31]
	v_cndmask_b32_e64 v29, 0, v18, vcc
	v_cndmask_b32_e64 v149, 0, v22, s[30:31]
	v_mul_f32_e64 v143, v110, v160
	v_mul_f32_e64 v144, v111, v160
	v_mul_f32_e64 v145, v156, v160
	v_mul_f32_e64 v146, v157, v160
	v_mul_f32_e64 v147, v158, v160
	v_mul_f32_e64 v148, v159, v160
	v_add_f32_e64 v150, v65, v29
	v_mov_b32_e32 v151, v25
	ds_write_b128 v23, v[140:143] offset:3072
	ds_write_b128 v23, v[144:147] offset:4096
	ds_write_b128 v23, v[148:151] offset:5120
	s_waitcnt lgkmcnt(0)
	s_barrier
	v_mov_b32_dpp v30, v6 wave_shr:1 row_mask:0xf bank_mask:0xf bound_ctrl:1
	v_mov_b32_dpp v31, v7 wave_shr:1 row_mask:0xf bank_mask:0xf bound_ctrl:1
	v_mov_b32_dpp v50, v6 wave_shl:1 row_mask:0xf bank_mask:0xf bound_ctrl:1
	v_mov_b32_dpp v51, v7 wave_shl:1 row_mask:0xf bank_mask:0xf bound_ctrl:1
	v_pk_mul_f32 v[60:61], v[6:7], v[12:13] op_sel_hi:[1,0]
	v_pk_mul_f32 v[62:63], v[6:7], v[12:13] op_sel:[0,1]
	v_pk_mul_f32 v[64:65], v[6:7], v[14:15] op_sel_hi:[1,0]
	v_pk_add_f32 v[82:83], v[6:7], v[30:31]
	v_pk_fma_f32 v[60:61], v[30:31], v[96:97], v[60:61] op_sel_hi:[1,0,1]
	v_pk_fma_f32 v[62:63], v[30:31], v[96:97], v[62:63] op_sel:[0,1,0]
	v_pk_fma_f32 v[64:65], v[30:31], v[98:99], v[64:65] op_sel_hi:[1,0,1]
	v_pk_add_f32 v[82:83], v[82:83], v[50:51]
	v_pk_fma_f32 v[60:61], v[50:51], v[100:101], v[60:61] op_sel_hi:[1,0,1]
	v_pk_fma_f32 v[62:63], v[50:51], v[100:101], v[62:63] op_sel:[0,1,0]
	v_pk_fma_f32 v[64:65], v[50:51], v[102:103], v[64:65] op_sel_hi:[1,0,1]
	v_pk_add_f32 v[30:31], v[38:39], v[82:83]
	v_pk_add_f32 v[38:39], v[94:95], v[60:61]
	v_pk_add_f32 v[50:51], v[56:57], v[62:63]
	v_pk_add_f32 v[56:57], v[66:67], v[64:65]
	v_pk_fma_f32 v[38:39], v[140:141], v[30:31], v[38:39] op_sel_hi:[0,1,1] neg_lo:[1,0,0] neg_hi:[1,0,0]
	v_pk_fma_f32 v[50:51], v[140:141], v[30:31], v[50:51] op_sel:[1,0,0] neg_lo:[1,0,0] neg_hi:[1,0,0]
	v_pk_fma_f32 v[56:57], v[142:143], v[30:31], v[56:57] op_sel_hi:[0,1,1] neg_lo:[1,0,0] neg_hi:[1,0,0]
	v_pk_mul_f32 v[66:67], v[142:143], v[38:39] op_sel:[1,0]
	v_pk_mul_f32 v[92:93], v[144:145], v[38:39] op_sel_hi:[0,1]
	v_pk_mul_f32 v[94:95], v[144:145], v[38:39] op_sel:[1,0]
	v_pk_fma_f32 v[66:67], v[144:145], v[50:51], v[66:67] op_sel_hi:[0,1,1]
	v_pk_fma_f32 v[92:93], v[146:147], v[50:51], v[92:93] op_sel_hi:[0,1,1]
	v_pk_fma_f32 v[94:95], v[146:147], v[50:51], v[94:95] op_sel:[1,0,0]
	v_pk_fma_f32 v[66:67], v[144:145], v[56:57], v[66:67] op_sel:[1,0,0]
	v_pk_fma_f32 v[92:93], v[146:147], v[56:57], v[92:93] op_sel:[1,0,0]
	v_pk_fma_f32 v[94:95], v[148:149], v[56:57], v[94:95] op_sel_hi:[0,1,1]
	v_pk_mul_f32 v[110:111], v[140:141], v[66:67] op_sel_hi:[0,1]
	v_pk_fma_f32 v[110:111], v[140:141], v[92:93], v[110:111] op_sel:[1,0,0]
	v_pk_fma_f32 v[110:111], v[142:143], v[94:95], v[110:111] op_sel_hi:[0,1,1]
	v_pk_fma_f32 v[110:111], v[148:149], v[30:31], v[110:111] op_sel:[1,0,0] neg_lo:[0,0,1] neg_hi:[0,0,1]
	v_cmp_eq_u32_e64 s[10:11], 6, v151
	v_cmp_eq_u32_e64 s[14:15], 7, v151
	v_pk_add_f32 v[30:31], v[58:59], v[66:67]
	v_pk_add_f32 v[38:39], v[88:89], v[92:93]
	v_pk_add_f32 v[50:51], v[108:109], v[94:95]
	v_pk_add_f32 v[56:57], v[118:119], v[110:111]
	v_pk_fma_f32 v[58:59], v[44:45], v[30:31], v[56:57] op_sel_hi:[0,1,1]
	v_pk_fma_f32 v[88:89], v[68:69], v[30:31], v[56:57] op_sel_hi:[0,1,1]
	v_pk_fma_f32 v[58:59], v[44:45], v[38:39], v[58:59] op_sel:[1,0,0]
	v_pk_fma_f32 v[88:89], v[68:69], v[38:39], v[88:89] op_sel:[1,0,0]
	v_pk_fma_f32 v[58:59], v[46:47], v[50:51], v[58:59] op_sel_hi:[0,1,1]
	v_pk_fma_f32 v[88:89], v[70:71], v[50:51], v[88:89] op_sel_hi:[0,1,1]
	v_pk_fma_f32 v[56:57], v[72:73], v[30:31], v[56:57] op_sel_hi:[0,1,1]
	v_pk_fma_f32 v[56:57], v[72:73], v[38:39], v[56:57] op_sel:[1,0,0]
	v_pk_fma_f32 v[56:57], v[74:75], v[50:51], v[56:57] op_sel_hi:[0,1,1]
	v_cndmask_b32_e64 v108, 0, v18, s[10:11]
	v_cndmask_b32_e64 v109, 0, v18, s[14:15]
	v_add_f32_dpp v56, v58, v56 wave_shl:1 row_mask:0xf bank_mask:0xf bound_ctrl:1
	v_add_f32_dpp v57, v59, v57 wave_shl:1 row_mask:0xf bank_mask:0xf bound_ctrl:1
	s_add_i32 s4, s34, 7
	s_cmpk_lt_i32 s4, 0x201
	s_cselect_b64 s[12:13], s[0:1], 0
	v_add_f32_dpp v56, v88, v56 wave_shr:1 row_mask:0xf bank_mask:0xf bound_ctrl:1
	v_add_f32_dpp v57, v89, v57 wave_shr:1 row_mask:0xf bank_mask:0xf bound_ctrl:1
	v_pk_fma_f32 v[56:57], v[48:49], v[150:151], v[56:57] op_sel_hi:[1,0,1] neg_lo:[0,0,1] neg_hi:[0,0,1]
	v_pk_add_f32 v[56:57], v[56:57], v[108:109] neg_lo:[0,1] neg_hi:[0,1]
	v_pk_mul_f32 v[118:119], v[56:57], v[56:57]
	v_add_f32_e32 v118, v118, v119
	v_cndmask_b32_e64 v119, 0, v118, s[12:13]
	v_add_f32_e32 v1, v1, v119
	s_waitcnt vmcnt(4)
	v_mov_b32_dpp v44, v32 wave_shr:1 row_mask:0xf bank_mask:0xf bound_ctrl:1
	v_mov_b32_dpp v45, v33 wave_shr:1 row_mask:0xf bank_mask:0xf bound_ctrl:1
	v_mov_b32_dpp v46, v34 wave_shr:1 row_mask:0xf bank_mask:0xf bound_ctrl:1
	v_mov_b32_dpp v48, v32 wave_shl:1 row_mask:0xf bank_mask:0xf bound_ctrl:1
	v_mov_b32_dpp v49, v33 wave_shl:1 row_mask:0xf bank_mask:0xf bound_ctrl:1
	v_mov_b32_dpp v50, v34 wave_shl:1 row_mask:0xf bank_mask:0xf bound_ctrl:1
	s_add_i32 s4, s34, 11
	s_cmpk_lt_u32 s4, 0x201
	s_cselect_b64 s[12:13], s[40:41], 0
	v_cmp_eq_u32_e64 s[14:15], s37, v3
	s_and_b64 s[14:15], s[14:15], s[12:13]
	v_cndmask_b32_e64 v25, 0, 1, s[14:15]
	v_mul_f32_e64 v30, v32, v32
	v_mul_f32_e64 v31, v32, v33
	v_mul_f32_e64 v38, v32, v34
	v_mul_f32_e64 v39, v33, v33
	v_mul_f32_e64 v56, v33, v34
	v_mul_f32_e64 v57, v34, v34
	v_or_b32_dpp v29, v25, v25 wave_shr:1 row_mask:0xf bank_mask:0xf bound_ctrl:1
	s_nop 1
	v_or_b32_dpp v29, v25, v29 wave_shl:1 row_mask:0xf bank_mask:0xf bound_ctrl:1
	s_nop 1
	v_or_b32_dpp v52, v29, v29 wave_shr:1 row_mask:0xf bank_mask:0xf bound_ctrl:1
	s_nop 1
	v_or_b32_dpp v52, v29, v52 wave_shl:1 row_mask:0xf bank_mask:0xf bound_ctrl:1
	v_or3_b32 v25, v52, v85, v128
	v_or3_b32 v25, v25, v129, v53
	s_add_i32 s4, s34, 8
	s_cmpk_lt_u32 s4, 0x1ff
	s_cselect_b64 s[12:13], s[42:43], 0
	v_cmp_ne_u32_e64 s[30:31], 0, v25
	s_and_b64 s[30:31], s[30:31], s[12:13]
	v_cndmask_b32_e64 v25, 0, 1.0, s[30:31]
	v_add_f32_e64 v58, v32, v44
	v_add_f32_e64 v59, v33, v45
	v_add_f32_e64 v68, v34, v46
	v_fma_f32 v30, v44, v44, v30
	v_fma_f32 v31, v44, v45, v31
	v_fma_f32 v38, v44, v46, v38
	v_fma_f32 v39, v45, v45, v39
	v_fma_f32 v56, v45, v46, v56
	v_fma_f32 v57, v46, v46, v57
	v_add_f32_dpp v75, v25, v25 wave_shr:1 row_mask:0xf bank_mask:0xf bound_ctrl:1
	v_add_f32_e64 v58, v58, v48
	v_add_f32_e64 v59, v59, v49
	v_add_f32_e64 v68, v68, v50
	v_fma_f32 v69, v48, v48, v30
	v_fma_f32 v70, v48, v49, v31
	v_fma_f32 v71, v48, v50, v38
	v_fma_f32 v72, v49, v49, v39
	v_fma_f32 v73, v49, v50, v56
	v_fma_f32 v74, v50, v50, v57
	v_add_f32_dpp v75, v25, v75 wave_shl:1 row_mask:0xf bank_mask:0xf bound_ctrl:1
	v_pk_add_f32 v[30:31], v[120:121], v[58:59]
	v_pk_add_f32 v[38:39], v[54:55], v[30:31]
	v_pk_add_f32 v[54:55], v[122:123], v[68:69]
	v_pk_add_f32 v[56:57], v[80:81], v[54:55]
	v_pk_add_f32 v[80:81], v[126:127], v[70:71]
	v_pk_add_f32 v[88:89], v[90:91], v[80:81]
	v_pk_add_f32 v[90:91], v[130:131], v[72:73]
	v_pk_add_f32 v[108:109], v[116:117], v[90:91]
	v_pk_add_f32 v[116:117], v[132:133], v[74:75]
	v_pk_add_f32 v[118:119], v[124:125], v[116:117]
	v_mul_f32_e64 v120, v38, v22
	v_mul_f32_e64 v121, v39, v22
	v_mul_f32_e64 v122, v56, v22
	v_fma_f32 v25, v57, v22, v26
	v_mul_f32_e64 v29, v88, v22
	v_mul_f32_e64 v84, v89, v22
	v_fma_f32 v130, v108, v22, v26
	v_mul_f32_e64 v131, v109, v22
	v_fma_f32 v132, v118, v22, v26
	v_fma_f32 v25, -v120, v120, v25
	v_fma_f32 v29, -v120, v121, v29
	v_fma_f32 v84, -v120, v122, v84
	v_fma_f32 v130, -v121, v121, v130
	v_fma_f32 v131, -v121, v122, v131
	v_fma_f32 v132, -v122, v122, v132
	v_mul_f32_e64 v133, v131, v131
	v_mul_f32_e64 v144, v29, v132
	v_mul_f32_e64 v145, v84, v130
	v_mul_f32_e64 v146, v84, v84
	v_mul_f32_e64 v147, v25, v131
	v_mul_f32_e64 v148, v29, v29
	v_fma_f32 v133, v130, v132, -v133
	v_fma_f32 v144, v84, v131, -v144
	v_fma_f32 v145, v29, v131, -v145
	v_fma_f32 v146, v25, v132, -v146
	v_fma_f32 v147, v29, v84, -v147
	v_fma_f32 v148, v25, v130, -v148
	v_mul_f32_e64 v149, v25, v133
	v_fma_f32 v149, v29, v144, v149
	v_fma_f32 v149, v84, v145, v149
	v_rcp_f32_e32 v149, v149
	v_cmp_ne_u32_e64 vcc, s37, v24
	v_mul_f32_e64 v149, v149, v22
	v_cndmask_b32_e64 v149, 0, v149, s[30:31]
	v_cndmask_b32_e64 v25, 0, v18, vcc
	v_cndmask_b32_e64 v141, 0, v22, s[30:31]
	v_mul_f32_e64 v123, v133, v149
	v_mul_f32_e64 v124, v144, v149
	v_mul_f32_e64 v125, v145, v149
	v_mul_f32_e64 v126, v146, v149
	v_mul_f32_e64 v127, v147, v149
	v_mul_f32_e64 v140, v148, v149
	v_add_f32_e64 v142, v119, v25
	v_mov_b32_e32 v143, v24
	ds_write_b128 v23, v[120:123]
	ds_write_b128 v23, v[124:127] offset:1024
	ds_write_b128 v23, v[140:143] offset:2048
	s_waitcnt lgkmcnt(0)
	s_barrier
	v_mov_b32_dpp v24, v20 wave_shr:1 row_mask:0xf bank_mask:0xf bound_ctrl:1
	v_mov_b32_dpp v25, v21 wave_shr:1 row_mask:0xf bank_mask:0xf bound_ctrl:1
	v_mov_b32_dpp v38, v20 wave_shl:1 row_mask:0xf bank_mask:0xf bound_ctrl:1
	v_mov_b32_dpp v39, v21 wave_shl:1 row_mask:0xf bank_mask:0xf bound_ctrl:1
	v_pk_mul_f32 v[56:57], v[20:21], v[32:33] op_sel_hi:[1,0]
	v_pk_mul_f32 v[88:89], v[20:21], v[32:33] op_sel:[0,1]
	v_pk_mul_f32 v[108:109], v[20:21], v[34:35] op_sel_hi:[1,0]
	v_pk_add_f32 v[118:119], v[20:21], v[24:25]
	v_pk_fma_f32 v[56:57], v[24:25], v[44:45], v[56:57] op_sel_hi:[1,0,1]
	v_pk_fma_f32 v[88:89], v[24:25], v[44:45], v[88:89] op_sel:[0,1,0]
	v_pk_fma_f32 v[108:109], v[24:25], v[46:47], v[108:109] op_sel_hi:[1,0,1]
	v_pk_add_f32 v[118:119], v[118:119], v[38:39]
	v_pk_fma_f32 v[56:57], v[38:39], v[48:49], v[56:57] op_sel_hi:[1,0,1]
	v_pk_fma_f32 v[88:89], v[38:39], v[48:49], v[88:89] op_sel:[0,1,0]
	v_pk_fma_f32 v[108:109], v[38:39], v[50:51], v[108:109] op_sel_hi:[1,0,1]
	v_pk_add_f32 v[24:25], v[82:83], v[118:119]
	v_pk_add_f32 v[38:39], v[138:139], v[24:25]
	v_pk_add_f32 v[82:83], v[60:61], v[56:57]
	v_pk_add_f32 v[130:131], v[112:113], v[82:83]
	v_pk_add_f32 v[60:61], v[62:63], v[88:89]
	v_pk_add_f32 v[112:113], v[134:135], v[60:61]
	v_pk_add_f32 v[62:63], v[64:65], v[108:109]
	v_pk_add_f32 v[132:133], v[136:137], v[62:63]
	v_pk_fma_f32 v[130:131], v[120:121], v[38:39], v[130:131] op_sel_hi:[0,1,1] neg_lo:[1,0,0] neg_hi:[1,0,0]
	v_pk_fma_f32 v[112:113], v[120:121], v[38:39], v[112:113] op_sel:[1,0,0] neg_lo:[1,0,0] neg_hi:[1,0,0]
	v_pk_fma_f32 v[132:133], v[122:123], v[38:39], v[132:133] op_sel_hi:[0,1,1] neg_lo:[1,0,0] neg_hi:[1,0,0]
	v_pk_mul_f32 v[64:65], v[122:123], v[130:131] op_sel:[1,0]
	v_pk_mul_f32 v[134:135], v[124:125], v[130:131] op_sel_hi:[0,1]
	v_pk_mul_f32 v[136:137], v[124:125], v[130:131] op_sel:[1,0]
	v_pk_fma_f32 v[64:65], v[124:125], v[112:113], v[64:65] op_sel_hi:[0,1,1]
	v_pk_fma_f32 v[134:135], v[126:127], v[112:113], v[134:135] op_sel_hi:[0,1,1]
	v_pk_fma_f32 v[136:137], v[126:127], v[112:113], v[136:137] op_sel:[1,0,0]
	v_pk_fma_f32 v[64:65], v[124:125], v[132:133], v[64:65] op_sel:[1,0,0]
	v_pk_fma_f32 v[134:135], v[126:127], v[132:133], v[134:135] op_sel:[1,0,0]
	v_pk_fma_f32 v[136:137], v[140:141], v[132:133], v[136:137] op_sel_hi:[0,1,1]
	v_pk_mul_f32 v[138:139], v[120:121], v[64:65] op_sel_hi:[0,1]
	v_pk_fma_f32 v[138:139], v[120:121], v[134:135], v[138:139] op_sel:[1,0,0]
	v_pk_fma_f32 v[138:139], v[122:123], v[136:137], v[138:139] op_sel_hi:[0,1,1]
	v_pk_fma_f32 v[138:139], v[140:141], v[38:39], v[138:139] op_sel:[1,0,0] neg_lo:[0,0,1] neg_hi:[0,0,1]
	v_cmp_eq_u32_e64 s[10:11], 6, v143
	v_cmp_eq_u32_e64 s[14:15], 7, v143
	v_pk_add_f32 v[38:39], v[66:67], v[64:65]
	v_pk_add_f32 v[112:113], v[86:87], v[38:39]
	v_pk_add_f32 v[66:67], v[92:93], v[134:135]
	v_pk_add_f32 v[86:87], v[114:115], v[66:67]
	v_pk_add_f32 v[92:93], v[94:95], v[136:137]
	v_pk_add_f32 v[114:115], v[152:153], v[92:93]
	v_pk_add_f32 v[94:95], v[110:111], v[138:139]
	v_pk_add_f32 v[130:131], v[154:155], v[94:95]
	v_pk_fma_f32 v[110:111], v[76:77], v[112:113], v[130:131] op_sel_hi:[0,1,1]
	v_pk_fma_f32 v[132:133], v[104:105], v[112:113], v[130:131] op_sel_hi:[0,1,1]
	v_pk_fma_f32 v[110:111], v[76:77], v[86:87], v[110:111] op_sel:[1,0,0]
	v_pk_fma_f32 v[132:133], v[104:105], v[86:87], v[132:133] op_sel:[1,0,0]
	v_pk_fma_f32 v[110:111], v[78:79], v[114:115], v[110:111] op_sel_hi:[0,1,1]
	v_pk_fma_f32 v[132:133], v[106:107], v[114:115], v[132:133] op_sel_hi:[0,1,1]
	v_pk_fma_f32 v[130:131], v[8:9], v[112:113], v[130:131] op_sel_hi:[0,1,1]
	v_pk_fma_f32 v[130:131], v[8:9], v[86:87], v[130:131] op_sel:[1,0,0]
	v_pk_fma_f32 v[130:131], v[10:11], v[114:115], v[130:131] op_sel_hi:[0,1,1]
	v_cndmask_b32_e64 v144, 0, v18, s[10:11]
	v_cndmask_b32_e64 v145, 0, v18, s[14:15]
	v_add_f32_dpp v130, v110, v130 wave_shl:1 row_mask:0xf bank_mask:0xf bound_ctrl:1
	v_add_f32_dpp v131, v111, v131 wave_shl:1 row_mask:0xf bank_mask:0xf bound_ctrl:1
	s_add_i32 s4, s34, 8
	s_cmpk_lt_i32 s4, 0x201
	s_cselect_b64 s[12:13], s[0:1], 0
	v_add_f32_dpp v130, v132, v130 wave_shr:1 row_mask:0xf bank_mask:0xf bound_ctrl:1
	v_add_f32_dpp v131, v133, v131 wave_shr:1 row_mask:0xf bank_mask:0xf bound_ctrl:1
	v_pk_fma_f32 v[130:131], v[4:5], v[142:143], v[130:131] op_sel_hi:[1,0,1] neg_lo:[0,0,1] neg_hi:[0,0,1]
	v_pk_add_f32 v[130:131], v[130:131], v[144:145] neg_lo:[0,1] neg_hi:[0,1]
	v_pk_mul_f32 v[146:147], v[130:131], v[130:131]
	v_add_f32_e32 v146, v146, v147
	v_cndmask_b32_e64 v147, 0, v146, s[12:13]
	v_add_f32_e32 v1, v1, v147
	s_waitcnt vmcnt(0)
	v_mov_b32_dpp v8, v40 wave_shr:1 row_mask:0xf bank_mask:0xf bound_ctrl:1
	v_mov_b32_dpp v9, v41 wave_shr:1 row_mask:0xf bank_mask:0xf bound_ctrl:1
	v_mov_b32_dpp v10, v42 wave_shr:1 row_mask:0xf bank_mask:0xf bound_ctrl:1
	v_mov_b32_dpp v76, v40 wave_shl:1 row_mask:0xf bank_mask:0xf bound_ctrl:1
	v_mov_b32_dpp v77, v41 wave_shl:1 row_mask:0xf bank_mask:0xf bound_ctrl:1
	v_mov_b32_dpp v78, v42 wave_shl:1 row_mask:0xf bank_mask:0xf bound_ctrl:1
	s_add_i32 s4, s34, 12
	s_cmpk_lt_u32 s4, 0x201
	s_cselect_b64 s[12:13], s[40:41], 0
	v_cmp_eq_u32_e64 s[14:15], s37, v16
	s_and_b64 s[14:15], s[14:15], s[12:13]
	v_cndmask_b32_e64 v29, 0, 1, s[14:15]
	v_mul_f32_e64 v4, v40, v40
	v_mul_f32_e64 v5, v40, v41
	v_mul_f32_e64 v86, v40, v42
	v_mul_f32_e64 v87, v41, v41
	v_mul_f32_e64 v104, v41, v42
	v_mul_f32_e64 v105, v42, v42
	v_or_b32_dpp v53, v29, v29 wave_shr:1 row_mask:0xf bank_mask:0xf bound_ctrl:1
	s_nop 1
	v_or_b32_dpp v53, v29, v53 wave_shl:1 row_mask:0xf bank_mask:0xf bound_ctrl:1
	s_nop 1
	v_or_b32_dpp v84, v53, v53 wave_shr:1 row_mask:0xf bank_mask:0xf bound_ctrl:1
	s_nop 1
	v_or_b32_dpp v84, v53, v84 wave_shl:1 row_mask:0xf bank_mask:0xf bound_ctrl:1
	v_or3_b32 v29, v84, v52, v85
	v_or3_b32 v29, v29, v128, v129
	s_add_i32 s4, s34, 9
	s_cmpk_lt_u32 s4, 0x1ff
	s_cselect_b64 s[12:13], s[42:43], 0
	v_cmp_ne_u32_e64 s[30:31], 0, v29
	s_and_b64 s[30:31], s[30:31], s[12:13]
	v_cndmask_b32_e64 v29, 0, 1.0, s[30:31]
	v_add_f32_e64 v106, v40, v8
	v_add_f32_e64 v107, v41, v9
	v_add_f32_e64 v110, v42, v10
	v_fma_f32 v4, v8, v8, v4
	v_fma_f32 v5, v8, v9, v5
	v_fma_f32 v86, v8, v10, v86
	v_fma_f32 v87, v9, v9, v87
	v_fma_f32 v104, v9, v10, v104
	v_fma_f32 v105, v10, v10, v105
	v_add_f32_dpp v121, v29, v29 wave_shr:1 row_mask:0xf bank_mask:0xf bound_ctrl:1
	v_add_f32_e64 v106, v106, v76
	v_add_f32_e64 v107, v107, v77
	v_add_f32_e64 v110, v110, v78
	v_fma_f32 v111, v76, v76, v4
	v_fma_f32 v112, v76, v77, v5
	v_fma_f32 v113, v76, v78, v86
	v_fma_f32 v114, v77, v77, v87
	v_fma_f32 v115, v77, v78, v104
	v_fma_f32 v120, v78, v78, v105
	v_add_f32_dpp v121, v29, v121 wave_shl:1 row_mask:0xf bank_mask:0xf bound_ctrl:1
	v_pk_add_f32 v[4:5], v[30:31], v[106:107]
	v_pk_add_f32 v[30:31], v[54:55], v[110:111]
	v_pk_add_f32 v[54:55], v[80:81], v[112:113]
	v_pk_add_f32 v[80:81], v[90:91], v[114:115]
	v_pk_add_f32 v[86:87], v[116:117], v[120:121]
	v_mul_f32_e64 v124, v4, v22
	v_mul_f32_e64 v125, v5, v22
	v_mul_f32_e64 v126, v30, v22
	v_fma_f32 v29, v31, v22, v26
	v_mul_f32_e64 v53, v54, v22
	v_mul_f32_e64 v90, v55, v22
	v_fma_f32 v91, v80, v22, v26
	v_mul_f32_e64 v104, v81, v22
	v_fma_f32 v105, v86, v22, v26
	v_fma_f32 v29, -v124, v124, v29
	v_fma_f32 v53, -v124, v125, v53
	v_fma_f32 v90, -v124, v126, v90
	v_fma_f32 v91, -v125, v125, v91
	v_fma_f32 v104, -v125, v126, v104
	v_fma_f32 v105, -v126, v126, v105
	v_mul_f32_e64 v116, v104, v104
	v_mul_f32_e64 v117, v53, v105
	v_mul_f32_e64 v122, v90, v91
	v_mul_f32_e64 v123, v90, v90
	v_mul_f32_e64 v130, v29, v104
	v_mul_f32_e64 v131, v53, v53
	v_fma_f32 v116, v91, v105, -v116
	v_fma_f32 v117, v90, v104, -v117
	v_fma_f32 v122, v53, v104, -v122
	v_fma_f32 v123, v29, v105, -v123
	v_fma_f32 v130, v53, v90, -v130
	v_fma_f32 v131, v29, v91, -v131
	v_mul_f32_e64 v132, v29, v116
	v_fma_f32 v132, v53, v117, v132
	v_fma_f32 v132, v90, v122, v132
	v_rcp_f32_e32 v132, v132
	v_cmp_ne_u32_e64 vcc, s37, v17
	v_mul_f32_e64 v132, v132, v22
	v_cndmask_b32_e64 v132, 0, v132, s[30:31]
	v_cndmask_b32_e64 v29, 0, v18, vcc
	v_cndmask_b32_e64 v145, 0, v22, s[30:31]
	v_mul_f32_e64 v127, v116, v132
	v_mul_f32_e64 v140, v117, v132
	v_mul_f32_e64 v141, v122, v132
	v_mul_f32_e64 v142, v123, v132
	v_mul_f32_e64 v143, v130, v132
	v_mul_f32_e64 v144, v131, v132
	v_add_f32_e64 v146, v87, v29
	v_mov_b32_e32 v147, v17
	ds_write_b128 v23, v[124:127] offset:3072
	ds_write_b128 v23, v[140:143] offset:4096
	ds_write_b128 v23, v[144:147] offset:5120
	s_waitcnt lgkmcnt(0)
	s_barrier
	v_mov_b32_dpp v4, v36 wave_shr:1 row_mask:0xf bank_mask:0xf bound_ctrl:1
	v_mov_b32_dpp v5, v37 wave_shr:1 row_mask:0xf bank_mask:0xf bound_ctrl:1
	v_mov_b32_dpp v30, v36 wave_shl:1 row_mask:0xf bank_mask:0xf bound_ctrl:1
	v_mov_b32_dpp v31, v37 wave_shl:1 row_mask:0xf bank_mask:0xf bound_ctrl:1
	v_pk_mul_f32 v[54:55], v[36:37], v[40:41] op_sel_hi:[1,0]
	v_pk_mul_f32 v[80:81], v[36:37], v[40:41] op_sel:[0,1]
	v_pk_mul_f32 v[86:87], v[36:37], v[42:43] op_sel_hi:[1,0]
	v_pk_add_f32 v[90:91], v[36:37], v[4:5]
	v_pk_fma_f32 v[54:55], v[4:5], v[8:9], v[54:55] op_sel_hi:[1,0,1]
	v_pk_fma_f32 v[80:81], v[4:5], v[8:9], v[80:81] op_sel:[0,1,0]
	v_pk_fma_f32 v[86:87], v[4:5], v[10:11], v[86:87] op_sel_hi:[1,0,1]
	v_pk_add_f32 v[90:91], v[90:91], v[30:31]
	v_pk_fma_f32 v[54:55], v[30:31], v[76:77], v[54:55] op_sel_hi:[1,0,1]
	v_pk_fma_f32 v[80:81], v[30:31], v[76:77], v[80:81] op_sel:[0,1,0]
	v_pk_fma_f32 v[86:87], v[30:31], v[78:79], v[86:87] op_sel_hi:[1,0,1]
	v_pk_add_f32 v[4:5], v[24:25], v[90:91]
	v_pk_add_f32 v[24:25], v[82:83], v[54:55]
	v_pk_add_f32 v[30:31], v[60:61], v[80:81]
	v_pk_add_f32 v[60:61], v[62:63], v[86:87]
	v_pk_fma_f32 v[24:25], v[124:125], v[4:5], v[24:25] op_sel_hi:[0,1,1] neg_lo:[1,0,0] neg_hi:[1,0,0]
	v_pk_fma_f32 v[30:31], v[124:125], v[4:5], v[30:31] op_sel:[1,0,0] neg_lo:[1,0,0] neg_hi:[1,0,0]
	v_pk_fma_f32 v[60:61], v[126:127], v[4:5], v[60:61] op_sel_hi:[0,1,1] neg_lo:[1,0,0] neg_hi:[1,0,0]
	v_pk_mul_f32 v[62:63], v[126:127], v[24:25] op_sel:[1,0]
	v_pk_mul_f32 v[82:83], v[140:141], v[24:25] op_sel_hi:[0,1]
	v_pk_mul_f32 v[104:105], v[140:141], v[24:25] op_sel:[1,0]
	v_pk_fma_f32 v[62:63], v[140:141], v[30:31], v[62:63] op_sel_hi:[0,1,1]
	v_pk_fma_f32 v[82:83], v[142:143], v[30:31], v[82:83] op_sel_hi:[0,1,1]
	v_pk_fma_f32 v[104:105], v[142:143], v[30:31], v[104:105] op_sel:[1,0,0]
	v_pk_fma_f32 v[62:63], v[140:141], v[60:61], v[62:63] op_sel:[1,0,0]
	v_pk_fma_f32 v[82:83], v[142:143], v[60:61], v[82:83] op_sel:[1,0,0]
	v_pk_fma_f32 v[104:105], v[144:145], v[60:61], v[104:105] op_sel_hi:[0,1,1]
	v_pk_mul_f32 v[116:117], v[124:125], v[62:63] op_sel_hi:[0,1]
	v_pk_fma_f32 v[116:117], v[124:125], v[82:83], v[116:117] op_sel:[1,0,0]
	v_pk_fma_f32 v[116:117], v[126:127], v[104:105], v[116:117] op_sel_hi:[0,1,1]
	v_pk_fma_f32 v[116:117], v[144:145], v[4:5], v[116:117] op_sel:[1,0,0] neg_lo:[0,0,1] neg_hi:[0,0,1]
	v_cmp_eq_u32_e64 s[10:11], 6, v147
	v_cmp_eq_u32_e64 s[14:15], 7, v147
	v_pk_add_f32 v[4:5], v[38:39], v[62:63]
	v_pk_add_f32 v[24:25], v[66:67], v[82:83]
	v_pk_add_f32 v[30:31], v[92:93], v[104:105]
	v_pk_add_f32 v[38:39], v[94:95], v[116:117]
	v_pk_fma_f32 v[60:61], v[96:97], v[4:5], v[38:39] op_sel_hi:[0,1,1]
	v_pk_fma_f32 v[66:67], v[100:101], v[4:5], v[38:39] op_sel_hi:[0,1,1]
	v_pk_fma_f32 v[60:61], v[96:97], v[24:25], v[60:61] op_sel:[1,0,0]
	v_pk_fma_f32 v[66:67], v[100:101], v[24:25], v[66:67] op_sel:[1,0,0]
	v_pk_fma_f32 v[60:61], v[98:99], v[30:31], v[60:61] op_sel_hi:[0,1,1]
	v_pk_fma_f32 v[66:67], v[102:103], v[30:31], v[66:67] op_sel_hi:[0,1,1]
	v_pk_fma_f32 v[38:39], v[12:13], v[4:5], v[38:39] op_sel_hi:[0,1,1]
	v_pk_fma_f32 v[38:39], v[12:13], v[24:25], v[38:39] op_sel:[1,0,0]
	v_pk_fma_f32 v[38:39], v[14:15], v[30:31], v[38:39] op_sel_hi:[0,1,1]
	v_cndmask_b32_e64 v92, 0, v18, s[10:11]
	v_cndmask_b32_e64 v93, 0, v18, s[14:15]
	v_add_f32_dpp v38, v60, v38 wave_shl:1 row_mask:0xf bank_mask:0xf bound_ctrl:1
	v_add_f32_dpp v39, v61, v39 wave_shl:1 row_mask:0xf bank_mask:0xf bound_ctrl:1
	s_add_i32 s4, s34, 9
	s_cmpk_lt_i32 s4, 0x201
	s_cselect_b64 s[12:13], s[0:1], 0
	v_add_f32_dpp v38, v66, v38 wave_shr:1 row_mask:0xf bank_mask:0xf bound_ctrl:1
	v_add_f32_dpp v39, v67, v39 wave_shr:1 row_mask:0xf bank_mask:0xf bound_ctrl:1
	v_pk_fma_f32 v[38:39], v[6:7], v[146:147], v[38:39] op_sel_hi:[1,0,1] neg_lo:[0,0,1] neg_hi:[0,0,1]
	v_pk_add_f32 v[38:39], v[38:39], v[92:93] neg_lo:[0,1] neg_hi:[0,1]
	v_pk_mul_f32 v[94:95], v[38:39], v[38:39]
	v_add_f32_e32 v94, v94, v95
	v_cndmask_b32_e64 v95, 0, v94, s[12:13]
	v_add_f32_e32 v1, v1, v95
	v_mov_b32_e32 v0, v1
	s_branch .LBB0_29
